# speedup vs baseline: 1.0152x; 1.0020x over previous
.LBB1_3:
	global_load_dwordx4 v[6:9], v164, s[94:95]
	global_load_dwordx4 v[2:5], v165, s[94:95]
	global_load_dwordx4 v[14:17], v166, s[94:95]
	global_load_dwordx4 v[10:13], v167, s[94:95]
	global_load_dwordx4 v[26:29], v168, s[94:95]
	global_load_dwordx4 v[22:25], v169, s[94:95]
	global_load_dwordx4 v[30:33], v170, s[94:95]
	global_load_dwordx4 v[34:37], v171, s[94:95]
	s_waitcnt lgkmcnt(0)
	v_mfma_f32_32x32x16_f16 a[0:15], v[18:21], v[74:77], a[0:15]
	s_add_i32 s31, s30, 1
	s_cmp_lg_u32 s30, 2
	s_cselect_b32 s91, s31, 0
	s_mul_i32 s30, s30, 0x9000
	s_mul_i32 s92, s91, 0x9000
	v_add_u32_e32 v147, s30, v141
	v_add_u32_e32 v146, s92, v141
	s_add_u32 s30, s35, s20
	s_addc_u32 s31, s84, s21
	s_load_dwordx16 s[68:83], s[30:31], 0x80
	s_load_dwordx16 s[52:67], s[30:31], 0x8080
	ds_read_b128 v[90:93], v145
	ds_read_b128 v[82:85], v145 offset:2048
	v_mfma_f32_32x32x16_f16 a[240:255], v[38:41], v[74:77], a[240:255]
	ds_read_b128 v[50:53], v147 offset:32
	v_pk_mul_f16 v148, v46, v136
	v_pk_mul_f16 v149, v42, v137
	v_pk_mul_f16 v150, v47, v136
	v_pk_mul_f16 v151, v43, v137
	v_mfma_f32_32x32x16_f16 a[16:31], v[18:21], v[126:129], a[16:31]
	ds_read_b128 v[54:57], v147 offset:4640
	v_pk_mul_f16 v152, v48, v136
	v_pk_mul_f16 v153, v44, v137
	v_pk_mul_f16 v154, v49, v136
	v_pk_mul_f16 v155, v45, v137
	v_mfma_f32_32x32x16_f16 a[224:239], v[38:41], v[126:129], a[224:239]
	ds_read_b128 v[58:61], v147 offset:9248
	v_pk_mul_f16 v156, v46, v140
	v_pk_mul_f16 v157, v42, v139
	v_pk_mul_f16 v158, v47, v140
	v_pk_mul_f16 v159, v43, v139
	v_mfma_f32_32x32x16_f16 a[32:47], v[18:21], v[122:125], a[32:47]
	ds_read_b128 v[62:65], v147 offset:13856
	v_pk_mul_f16 v160, v48, v140
	v_pk_mul_f16 v161, v44, v139
	v_pk_mul_f16 v162, v49, v140
	v_pk_mul_f16 v163, v45, v139
	v_mfma_f32_32x32x16_f16 a[208:223], v[38:41], v[122:125], a[208:223]
	ds_read_b128 v[66:69], v147 offset:18464
	v_pk_max_f16 v148, v148, v149
	v_pk_max_f16 v150, v150, v151
	v_pk_max_f16 v152, v152, v153
	v_pk_max_f16 v154, v154, v155
	v_mfma_f32_32x32x16_f16 a[48:63], v[18:21], v[118:121], a[48:63]
	ds_read_b128 v[70:73], v147 offset:23072
	v_pk_max_f16 v156, v156, v157
	v_pk_max_f16 v158, v158, v159
	v_pk_max_f16 v160, v160, v161
	v_pk_max_f16 v162, v162, v163
	v_mfma_f32_32x32x16_f16 a[192:207], v[38:41], v[118:121], a[192:207]
	ds_read_b128 v[78:81], v147 offset:27680
	v_cndmask_b32_e64 v114, v1, v148, s[36:37]
	s_mov_b64 vcc, s[38:39]
	v_cndmask_b32_sdwa v114, v1, v148, vcc dst_sel:WORD_1 dst_unused:UNUSED_PRESERVE src0_sel:WORD_1 src1_sel:WORD_1
	v_cndmask_b32_e64 v115, v1, v150, s[40:41]
	s_mov_b64 vcc, s[42:43]
	v_cndmask_b32_sdwa v115, v1, v150, vcc dst_sel:WORD_1 dst_unused:UNUSED_PRESERVE src0_sel:WORD_1 src1_sel:WORD_1
	v_mfma_f32_32x32x16_f16 a[64:79], v[18:21], v[106:109], a[64:79]
	ds_read_b128 v[102:105], v147 offset:32288
	v_cndmask_b32_e64 v116, v1, v152, s[44:45]
	s_mov_b64 vcc, s[46:47]
	v_cndmask_b32_sdwa v116, v1, v152, vcc dst_sel:WORD_1 dst_unused:UNUSED_PRESERVE src0_sel:WORD_1 src1_sel:WORD_1
	v_cndmask_b32_e64 v117, v1, v154, s[48:49]
	s_mov_b64 vcc, s[50:51]
	v_cndmask_b32_sdwa v117, v1, v154, vcc dst_sel:WORD_1 dst_unused:UNUSED_PRESERVE src0_sel:WORD_1 src1_sel:WORD_1
	v_mfma_f32_32x32x16_f16 a[176:191], v[38:41], v[106:109], a[176:191]
	v_cndmask_b32_e64 v110, v138, v156, s[4:5]
	s_mov_b64 vcc, s[6:7]
	v_cndmask_b32_sdwa v110, v138, v156, vcc dst_sel:WORD_1 dst_unused:UNUSED_PRESERVE src0_sel:WORD_1 src1_sel:WORD_1
	v_cndmask_b32_e64 v111, v138, v158, s[8:9]
	s_mov_b64 vcc, s[10:11]
	v_cndmask_b32_sdwa v111, v138, v158, vcc dst_sel:WORD_1 dst_unused:UNUSED_PRESERVE src0_sel:WORD_1 src1_sel:WORD_1
	v_mfma_f32_32x32x16_f16 a[112:127], v[18:21], v[98:101], a[112:127]
	v_cndmask_b32_e64 v112, v138, v160, s[12:13]
	s_mov_b64 vcc, s[14:15]
	v_cndmask_b32_sdwa v112, v138, v160, vcc dst_sel:WORD_1 dst_unused:UNUSED_PRESERVE src0_sel:WORD_1 src1_sel:WORD_1
	v_cndmask_b32_e64 v113, v138, v162, s[16:17]
	s_mov_b64 vcc, s[18:19]
	v_cndmask_b32_sdwa v113, v138, v162, vcc dst_sel:WORD_1 dst_unused:UNUSED_PRESERVE src0_sel:WORD_1 src1_sel:WORD_1
	v_mfma_f32_32x32x16_f16 a[160:175], v[38:41], v[98:101], a[160:175]
	v_pk_add_f16 v148, v115, v114
	v_pk_add_f16 v149, v116, v117
	v_mfma_f32_32x32x16_f16 a[128:143], v[18:21], v[94:97], a[128:143]
	v_pk_add_f16 v150, v111, v110
	v_pk_add_f16 v151, v112, v113
	v_mfma_f32_32x32x16_f16 a[144:159], v[38:41], v[94:97], a[144:159]
	v_pk_add_f16 v148, v148, v149
	v_pk_add_f16 v150, v150, v151
	v_mfma_f32_32x32x16_f16 a[80:95], v[18:21], v[86:89], a[80:95]
	v_dot2c_f32_f16_e32 v134, 0x3c003c00, v148
	v_dot2c_f32_f16_e32 v135, 0x3c003c00, v150
	v_mfma_f32_32x32x16_f16 a[96:111], v[38:41], v[86:89], a[96:111]
	s_waitcnt lgkmcnt(0)
	v_mfma_f32_32x32x16_f16 a[0:15], v[114:117], v[50:53], a[0:15]
	s_load_dwordx16 s[36:51], s[30:31], 0xc0
	s_load_dwordx16 s[4:19], s[30:31], 0x80c0
	ds_read_b128 v[46:49], v145 offset:32
	ds_read_b128 v[42:45], v145 offset:2080
	v_mfma_f32_32x32x16_f16 a[240:255], v[110:113], v[50:53], a[240:255]
	ds_read_b128 v[74:77], v147 offset:64
	v_pk_mul_f16 v148, v90, v136
	v_pk_mul_f16 v149, v82, v137
	v_pk_mul_f16 v150, v91, v136
	v_pk_mul_f16 v151, v83, v137
	v_mfma_f32_32x32x16_f16 a[16:31], v[114:117], v[54:57], a[16:31]
	ds_read_b128 v[126:129], v147 offset:4672
	v_pk_mul_f16 v152, v92, v136
	v_pk_mul_f16 v153, v84, v137
	v_pk_mul_f16 v154, v93, v136
	v_pk_mul_f16 v155, v85, v137
	v_mfma_f32_32x32x16_f16 a[224:239], v[110:113], v[54:57], a[224:239]
	ds_read_b128 v[122:125], v147 offset:9280
	v_pk_mul_f16 v156, v90, v140
	v_pk_mul_f16 v157, v82, v139
	v_pk_mul_f16 v158, v91, v140
	v_pk_mul_f16 v159, v83, v139
	v_mfma_f32_32x32x16_f16 a[32:47], v[114:117], v[58:61], a[32:47]
	ds_read_b128 v[118:121], v147 offset:13888
	v_pk_mul_f16 v160, v92, v140
	v_pk_mul_f16 v161, v84, v139
	v_pk_mul_f16 v162, v93, v140
	v_pk_mul_f16 v163, v85, v139
	v_mfma_f32_32x32x16_f16 a[208:223], v[110:113], v[58:61], a[208:223]
	ds_read_b128 v[106:109], v147 offset:18496
	v_pk_max_f16 v148, v148, v149
	v_pk_max_f16 v150, v150, v151
	v_pk_max_f16 v152, v152, v153
	v_pk_max_f16 v154, v154, v155
	v_mfma_f32_32x32x16_f16 a[48:63], v[114:117], v[62:65], a[48:63]
	ds_read_b128 v[98:101], v147 offset:23104
	v_pk_max_f16 v156, v156, v157
	v_pk_max_f16 v158, v158, v159
	v_pk_max_f16 v160, v160, v161
	v_pk_max_f16 v162, v162, v163
	v_mfma_f32_32x32x16_f16 a[192:207], v[110:113], v[62:65], a[192:207]
	ds_read_b128 v[94:97], v147 offset:27712
	v_cndmask_b32_e64 v18, v1, v148, s[68:69]
	s_mov_b64 vcc, s[70:71]
	v_cndmask_b32_sdwa v18, v1, v148, vcc dst_sel:WORD_1 dst_unused:UNUSED_PRESERVE src0_sel:WORD_1 src1_sel:WORD_1
	v_cndmask_b32_e64 v19, v1, v150, s[72:73]
	s_mov_b64 vcc, s[74:75]
	v_cndmask_b32_sdwa v19, v1, v150, vcc dst_sel:WORD_1 dst_unused:UNUSED_PRESERVE src0_sel:WORD_1 src1_sel:WORD_1
	v_mfma_f32_32x32x16_f16 a[64:79], v[114:117], v[66:69], a[64:79]
	ds_read_b128 v[86:89], v147 offset:32320
	v_cndmask_b32_e64 v20, v1, v152, s[76:77]
	s_mov_b64 vcc, s[78:79]
	v_cndmask_b32_sdwa v20, v1, v152, vcc dst_sel:WORD_1 dst_unused:UNUSED_PRESERVE src0_sel:WORD_1 src1_sel:WORD_1
	v_cndmask_b32_e64 v21, v1, v154, s[80:81]
	s_mov_b64 vcc, s[82:83]
	v_cndmask_b32_sdwa v21, v1, v154, vcc dst_sel:WORD_1 dst_unused:UNUSED_PRESERVE src0_sel:WORD_1 src1_sel:WORD_1
	v_mfma_f32_32x32x16_f16 a[176:191], v[110:113], v[66:69], a[176:191]
	v_cndmask_b32_e64 v38, v138, v156, s[52:53]
	s_mov_b64 vcc, s[54:55]
	v_cndmask_b32_sdwa v38, v138, v156, vcc dst_sel:WORD_1 dst_unused:UNUSED_PRESERVE src0_sel:WORD_1 src1_sel:WORD_1
	v_cndmask_b32_e64 v39, v138, v158, s[56:57]
	s_mov_b64 vcc, s[58:59]
	v_cndmask_b32_sdwa v39, v138, v158, vcc dst_sel:WORD_1 dst_unused:UNUSED_PRESERVE src0_sel:WORD_1 src1_sel:WORD_1
	v_mfma_f32_32x32x16_f16 a[112:127], v[114:117], v[70:73], a[112:127]
	v_cndmask_b32_e64 v40, v138, v160, s[60:61]
	s_mov_b64 vcc, s[62:63]
	v_cndmask_b32_sdwa v40, v138, v160, vcc dst_sel:WORD_1 dst_unused:UNUSED_PRESERVE src0_sel:WORD_1 src1_sel:WORD_1
	v_cndmask_b32_e64 v41, v138, v162, s[64:65]
	s_mov_b64 vcc, s[66:67]
	v_cndmask_b32_sdwa v41, v138, v162, vcc dst_sel:WORD_1 dst_unused:UNUSED_PRESERVE src0_sel:WORD_1 src1_sel:WORD_1
	v_mfma_f32_32x32x16_f16 a[160:175], v[110:113], v[70:73], a[160:175]
	v_pk_add_f16 v148, v19, v18
	v_pk_add_f16 v149, v20, v21
	v_mfma_f32_32x32x16_f16 a[128:143], v[114:117], v[78:81], a[128:143]
	v_pk_add_f16 v150, v39, v38
	v_pk_add_f16 v151, v40, v41
	v_mfma_f32_32x32x16_f16 a[144:159], v[110:113], v[78:81], a[144:159]
	v_pk_add_f16 v148, v148, v149
	v_pk_add_f16 v150, v150, v151
	v_mfma_f32_32x32x16_f16 a[80:95], v[114:117], v[102:105], a[80:95]
	v_dot2c_f32_f16_e32 v134, 0x3c003c00, v148
	v_dot2c_f32_f16_e32 v135, 0x3c003c00, v150
	v_mfma_f32_32x32x16_f16 a[96:111], v[110:113], v[102:105], a[96:111]
	s_waitcnt lgkmcnt(0)
	v_mfma_f32_32x32x16_f16 a[0:15], v[18:21], v[74:77], a[0:15]
	s_load_dwordx16 s[68:83], s[30:31], 0x100
	s_load_dwordx16 s[52:67], s[30:31], 0x8100
	ds_read_b128 v[90:93], v145 offset:64
	ds_read_b128 v[82:85], v145 offset:2112
	v_mfma_f32_32x32x16_f16 a[240:255], v[38:41], v[74:77], a[240:255]
	ds_read_b128 v[50:53], v147 offset:96
	v_pk_mul_f16 v148, v46, v136
	v_pk_mul_f16 v149, v42, v137
	v_pk_mul_f16 v150, v47, v136
	v_pk_mul_f16 v151, v43, v137
	v_mfma_f32_32x32x16_f16 a[16:31], v[18:21], v[126:129], a[16:31]
	ds_read_b128 v[54:57], v147 offset:4704
	v_pk_mul_f16 v152, v48, v136
	v_pk_mul_f16 v153, v44, v137
	v_pk_mul_f16 v154, v49, v136
	v_pk_mul_f16 v155, v45, v137
	v_mfma_f32_32x32x16_f16 a[224:239], v[38:41], v[126:129], a[224:239]
	ds_read_b128 v[58:61], v147 offset:9312
	v_pk_mul_f16 v156, v46, v140
	v_pk_mul_f16 v157, v42, v139
	v_pk_mul_f16 v158, v47, v140
	v_pk_mul_f16 v159, v43, v139
	v_mfma_f32_32x32x16_f16 a[32:47], v[18:21], v[122:125], a[32:47]
	ds_read_b128 v[62:65], v147 offset:13920
	v_pk_mul_f16 v160, v48, v140
	v_pk_mul_f16 v161, v44, v139
	v_pk_mul_f16 v162, v49, v140
	v_pk_mul_f16 v163, v45, v139
	v_mfma_f32_32x32x16_f16 a[208:223], v[38:41], v[122:125], a[208:223]
	ds_read_b128 v[66:69], v147 offset:18528
	v_pk_max_f16 v148, v148, v149
	v_pk_max_f16 v150, v150, v151
	v_pk_max_f16 v152, v152, v153
	v_pk_max_f16 v154, v154, v155
	v_mfma_f32_32x32x16_f16 a[48:63], v[18:21], v[118:121], a[48:63]
	ds_read_b128 v[70:73], v147 offset:23136
	v_pk_max_f16 v156, v156, v157
	v_pk_max_f16 v158, v158, v159
	v_pk_max_f16 v160, v160, v161
	v_pk_max_f16 v162, v162, v163
	v_mfma_f32_32x32x16_f16 a[192:207], v[38:41], v[118:121], a[192:207]
	ds_read_b128 v[78:81], v147 offset:27744
	v_cndmask_b32_e64 v114, v1, v148, s[36:37]
	s_mov_b64 vcc, s[38:39]
	v_cndmask_b32_sdwa v114, v1, v148, vcc dst_sel:WORD_1 dst_unused:UNUSED_PRESERVE src0_sel:WORD_1 src1_sel:WORD_1
	v_cndmask_b32_e64 v115, v1, v150, s[40:41]
	s_mov_b64 vcc, s[42:43]
	v_cndmask_b32_sdwa v115, v1, v150, vcc dst_sel:WORD_1 dst_unused:UNUSED_PRESERVE src0_sel:WORD_1 src1_sel:WORD_1
	v_mfma_f32_32x32x16_f16 a[64:79], v[18:21], v[106:109], a[64:79]
	ds_read_b128 v[102:105], v147 offset:32352
	v_cndmask_b32_e64 v116, v1, v152, s[44:45]
	s_mov_b64 vcc, s[46:47]
	v_cndmask_b32_sdwa v116, v1, v152, vcc dst_sel:WORD_1 dst_unused:UNUSED_PRESERVE src0_sel:WORD_1 src1_sel:WORD_1
	v_cndmask_b32_e64 v117, v1, v154, s[48:49]
	s_mov_b64 vcc, s[50:51]
	v_cndmask_b32_sdwa v117, v1, v154, vcc dst_sel:WORD_1 dst_unused:UNUSED_PRESERVE src0_sel:WORD_1 src1_sel:WORD_1
	v_mfma_f32_32x32x16_f16 a[176:191], v[38:41], v[106:109], a[176:191]
	v_cndmask_b32_e64 v110, v138, v156, s[4:5]
	s_mov_b64 vcc, s[6:7]
	v_cndmask_b32_sdwa v110, v138, v156, vcc dst_sel:WORD_1 dst_unused:UNUSED_PRESERVE src0_sel:WORD_1 src1_sel:WORD_1
	v_cndmask_b32_e64 v111, v138, v158, s[8:9]
	s_mov_b64 vcc, s[10:11]
	v_cndmask_b32_sdwa v111, v138, v158, vcc dst_sel:WORD_1 dst_unused:UNUSED_PRESERVE src0_sel:WORD_1 src1_sel:WORD_1
	v_mfma_f32_32x32x16_f16 a[112:127], v[18:21], v[98:101], a[112:127]
	v_cndmask_b32_e64 v112, v138, v160, s[12:13]
	s_mov_b64 vcc, s[14:15]
	v_cndmask_b32_sdwa v112, v138, v160, vcc dst_sel:WORD_1 dst_unused:UNUSED_PRESERVE src0_sel:WORD_1 src1_sel:WORD_1
	v_cndmask_b32_e64 v113, v138, v162, s[16:17]
	s_mov_b64 vcc, s[18:19]
	v_cndmask_b32_sdwa v113, v138, v162, vcc dst_sel:WORD_1 dst_unused:UNUSED_PRESERVE src0_sel:WORD_1 src1_sel:WORD_1
	v_mfma_f32_32x32x16_f16 a[160:175], v[38:41], v[98:101], a[160:175]
	v_pk_add_f16 v148, v115, v114
	v_pk_add_f16 v149, v116, v117
	v_mfma_f32_32x32x16_f16 a[128:143], v[18:21], v[94:97], a[128:143]
	v_pk_add_f16 v150, v111, v110
	v_pk_add_f16 v151, v112, v113
	v_mfma_f32_32x32x16_f16 a[144:159], v[38:41], v[94:97], a[144:159]
	v_pk_add_f16 v148, v148, v149
	v_pk_add_f16 v150, v150, v151
	v_mfma_f32_32x32x16_f16 a[80:95], v[18:21], v[86:89], a[80:95]
	v_dot2c_f32_f16_e32 v134, 0x3c003c00, v148
	v_dot2c_f32_f16_e32 v135, 0x3c003c00, v150
	v_mfma_f32_32x32x16_f16 a[96:111], v[38:41], v[86:89], a[96:111]
	s_waitcnt lgkmcnt(0)
	v_mfma_f32_32x32x16_f16 a[0:15], v[114:117], v[50:53], a[0:15]
	s_load_dwordx16 s[36:51], s[30:31], 0x140
	s_load_dwordx16 s[4:19], s[30:31], 0x8140
	ds_read_b128 v[46:49], v145 offset:96
	ds_read_b128 v[42:45], v145 offset:2144
	v_mfma_f32_32x32x16_f16 a[240:255], v[110:113], v[50:53], a[240:255]
	ds_read_b128 v[74:77], v146
	v_pk_mul_f16 v148, v90, v136
	v_pk_mul_f16 v149, v82, v137
	v_pk_mul_f16 v150, v91, v136
	v_pk_mul_f16 v151, v83, v137
	v_mfma_f32_32x32x16_f16 a[16:31], v[114:117], v[54:57], a[16:31]
	ds_read_b128 v[126:129], v146 offset:4608
	v_pk_mul_f16 v152, v92, v136
	v_pk_mul_f16 v153, v84, v137
	v_pk_mul_f16 v154, v93, v136
	v_pk_mul_f16 v155, v85, v137
	v_mfma_f32_32x32x16_f16 a[224:239], v[110:113], v[54:57], a[224:239]
	ds_read_b128 v[122:125], v146 offset:9216
	v_pk_mul_f16 v156, v90, v140
	v_pk_mul_f16 v157, v82, v139
	v_pk_mul_f16 v158, v91, v140
	v_pk_mul_f16 v159, v83, v139
	v_mfma_f32_32x32x16_f16 a[32:47], v[114:117], v[58:61], a[32:47]
	ds_read_b128 v[118:121], v146 offset:13824
	v_pk_mul_f16 v160, v92, v140
	v_pk_mul_f16 v161, v84, v139
	v_pk_mul_f16 v162, v93, v140
	v_pk_mul_f16 v163, v85, v139
	v_mfma_f32_32x32x16_f16 a[208:223], v[110:113], v[58:61], a[208:223]
	ds_read_b128 v[106:109], v146 offset:18432
	v_pk_max_f16 v148, v148, v149
	v_pk_max_f16 v150, v150, v151
	v_pk_max_f16 v152, v152, v153
	v_pk_max_f16 v154, v154, v155
	v_mfma_f32_32x32x16_f16 a[48:63], v[114:117], v[62:65], a[48:63]
	ds_read_b128 v[98:101], v146 offset:23040
	v_pk_max_f16 v156, v156, v157
	v_pk_max_f16 v158, v158, v159
	v_pk_max_f16 v160, v160, v161
	v_pk_max_f16 v162, v162, v163
	v_mfma_f32_32x32x16_f16 a[192:207], v[110:113], v[62:65], a[192:207]
	ds_read_b128 v[94:97], v146 offset:27648
	v_cndmask_b32_e64 v18, v1, v148, s[68:69]
	s_mov_b64 vcc, s[70:71]
	v_cndmask_b32_sdwa v18, v1, v148, vcc dst_sel:WORD_1 dst_unused:UNUSED_PRESERVE src0_sel:WORD_1 src1_sel:WORD_1
	v_cndmask_b32_e64 v19, v1, v150, s[72:73]
	s_mov_b64 vcc, s[74:75]
	v_cndmask_b32_sdwa v19, v1, v150, vcc dst_sel:WORD_1 dst_unused:UNUSED_PRESERVE src0_sel:WORD_1 src1_sel:WORD_1
	v_mfma_f32_32x32x16_f16 a[64:79], v[114:117], v[66:69], a[64:79]
	ds_read_b128 v[86:89], v146 offset:32256
	v_cndmask_b32_e64 v20, v1, v152, s[76:77]
	s_mov_b64 vcc, s[78:79]
	v_cndmask_b32_sdwa v20, v1, v152, vcc dst_sel:WORD_1 dst_unused:UNUSED_PRESERVE src0_sel:WORD_1 src1_sel:WORD_1
	v_cndmask_b32_e64 v21, v1, v154, s[80:81]
	s_mov_b64 vcc, s[82:83]
	v_cndmask_b32_sdwa v21, v1, v154, vcc dst_sel:WORD_1 dst_unused:UNUSED_PRESERVE src0_sel:WORD_1 src1_sel:WORD_1
	v_mfma_f32_32x32x16_f16 a[176:191], v[110:113], v[66:69], a[176:191]
	v_cndmask_b32_e64 v38, v138, v156, s[52:53]
	s_mov_b64 vcc, s[54:55]
	v_cndmask_b32_sdwa v38, v138, v156, vcc dst_sel:WORD_1 dst_unused:UNUSED_PRESERVE src0_sel:WORD_1 src1_sel:WORD_1
	v_cndmask_b32_e64 v39, v138, v158, s[56:57]
	s_mov_b64 vcc, s[58:59]
	v_cndmask_b32_sdwa v39, v138, v158, vcc dst_sel:WORD_1 dst_unused:UNUSED_PRESERVE src0_sel:WORD_1 src1_sel:WORD_1
	v_mfma_f32_32x32x16_f16 a[112:127], v[114:117], v[70:73], a[112:127]
	v_cndmask_b32_e64 v40, v138, v160, s[60:61]
	s_mov_b64 vcc, s[62:63]
	v_cndmask_b32_sdwa v40, v138, v160, vcc dst_sel:WORD_1 dst_unused:UNUSED_PRESERVE src0_sel:WORD_1 src1_sel:WORD_1
	v_cndmask_b32_e64 v41, v138, v162, s[64:65]
	s_mov_b64 vcc, s[66:67]
	v_cndmask_b32_sdwa v41, v138, v162, vcc dst_sel:WORD_1 dst_unused:UNUSED_PRESERVE src0_sel:WORD_1 src1_sel:WORD_1
	v_mfma_f32_32x32x16_f16 a[160:175], v[110:113], v[70:73], a[160:175]
	v_pk_add_f16 v148, v19, v18
	v_pk_add_f16 v149, v20, v21
	v_mfma_f32_32x32x16_f16 a[128:143], v[114:117], v[78:81], a[128:143]
	v_pk_add_f16 v150, v39, v38
	v_pk_add_f16 v151, v40, v41
	v_mfma_f32_32x32x16_f16 a[144:159], v[110:113], v[78:81], a[144:159]
	v_pk_add_f16 v148, v148, v149
	v_pk_add_f16 v150, v150, v151
	v_mfma_f32_32x32x16_f16 a[80:95], v[114:117], v[102:105], a[80:95]
	v_dot2c_f32_f16_e32 v134, 0x3c003c00, v148
	v_dot2c_f32_f16_e32 v135, 0x3c003c00, v150
	v_mfma_f32_32x32x16_f16 a[96:111], v[110:113], v[102:105], a[96:111]
	s_add_i32 s92, s92, 0x9000
	s_cmp_lg_u32 s91, 2
	s_cselect_b32 s30, s92, 0
	s_add_u32 s20, s20, 0x100
	s_addc_u32 s21, s21, 0
	v_add_u32_e32 v50, s30, v144
	s_add_u32 s94, s94, 0x8000
	s_addc_u32 s95, s95, 0
	v_add_u32_e32 v145, 0x80, v145
	s_cmpk_eq_i32 s20, 0xf00
	s_mov_b32 s30, s91
	s_waitcnt vmcnt(6)
	s_waitcnt vmcnt(5)
	s_waitcnt vmcnt(4)
	s_waitcnt vmcnt(3)
	s_waitcnt vmcnt(2)
	s_waitcnt vmcnt(1)
	s_waitcnt vmcnt(0)
	ds_write_b128 v50, v[6:9]
	ds_write_b128 v50, v[2:5] offset:4608
	ds_write_b128 v50, v[14:17] offset:9216
	ds_write_b128 v50, v[10:13] offset:13824
	ds_write_b128 v50, v[26:29] offset:18432
	ds_write_b128 v50, v[22:25] offset:23040
	ds_write_b128 v50, v[30:33] offset:27648
	ds_write_b128 v50, v[34:37] offset:32256
	s_waitcnt lgkmcnt(0)
	s_barrier
	s_cbranch_scc0 .LBB1_3
	v_accvgpr_read_b32 v175, a95
	v_accvgpr_read_b32 v174, a94
	v_accvgpr_read_b32 v173, a93
	v_accvgpr_read_b32 v172, a92
	v_accvgpr_read_b32 v171, a91
	v_accvgpr_read_b32 v170, a90
	v_accvgpr_read_b32 v169, a89
	v_accvgpr_read_b32 v168, a88
	v_accvgpr_read_b32 v167, a87
	v_accvgpr_read_b32 v166, a86
	v_accvgpr_read_b32 v165, a85
	v_accvgpr_read_b32 v164, a84
	v_accvgpr_read_b32 v163, a83
	v_accvgpr_read_b32 v162, a82
	v_accvgpr_read_b32 v161, a81
	v_accvgpr_read_b32 v160, a80
	v_mfma_f32_32x32x16_f16 a[80:95], v[18:21], v[74:77], a[0:15]
	s_nop 11
	v_accvgpr_read_b32 v159, a95
	v_accvgpr_read_b32 v158, a94
	v_accvgpr_read_b32 v157, a93
	v_accvgpr_read_b32 v156, a92
	v_accvgpr_read_b32 v155, a91
	v_accvgpr_read_b32 v154, a90
	v_accvgpr_read_b32 v153, a89
	v_accvgpr_read_b32 v152, a88
	v_accvgpr_read_b32 v151, a87
	v_accvgpr_read_b32 v150, a86
	v_accvgpr_read_b32 v149, a85
	v_accvgpr_read_b32 v148, a84
	v_accvgpr_read_b32 v147, a83
	v_accvgpr_read_b32 v146, a82
	v_accvgpr_read_b32 v145, a81
	v_accvgpr_read_b32 v144, a80
	ds_read_b128 v[2:5], v141 offset:32288
	ds_read_b128 v[82:85], v141 offset:32
	ds_read_b128 v[58:61], v141 offset:4640
	ds_read_b128 v[50:53], v141 offset:9248
	ds_read_b128 v[26:29], v141 offset:13856
	ds_read_b128 v[22:25], v141 offset:18464
	ds_read_b128 v[14:17], v141 offset:23072
	ds_read_b128 v[10:13], v141 offset:27680
	s_load_dwordx16 s[68:83], s[0:1], 0xf80
	s_load_dwordx16 s[52:67], s[0:1], 0x8f80
	ds_read_b128 v[54:57], v142 offset:1984
	ds_read_b128 v[34:37], v143 offset:1984
	v_mfma_f32_32x32x16_f16 a[0:15], v[38:41], v[74:77], a[240:255]
	v_pk_mul_f16 v6, v46, v136
	v_pk_mul_f16 v7, v42, v137
	s_mov_b32 s20, 0x7060100
	v_pk_max_f16 v6, v6, v7
	s_nop 0
	v_cndmask_b32_e64 v7, v1, v6, s[36:37]
	v_mfma_f32_32x32x16_f16 a[240:255], v[18:21], v[126:129], a[16:31]
	v_cndmask_b32_e64 v6, v1, v6, s[38:39]
	v_perm_b32 v74, v6, v7, s20
	v_pk_mul_f16 v6, v47, v136
	v_pk_mul_f16 v7, v43, v137
	v_mfma_f32_32x32x16_f16 a[16:31], v[38:41], v[126:129], a[224:239]
	v_pk_max_f16 v6, v6, v7
	s_nop 0
	v_cndmask_b32_e64 v7, v1, v6, s[40:41]
	v_cndmask_b32_e64 v6, v1, v6, s[42:43]
	v_perm_b32 v75, v6, v7, s20
	v_mfma_f32_32x32x16_f16 a[224:239], v[18:21], v[122:125], a[32:47]
	v_pk_mul_f16 v6, v48, v136
	v_pk_mul_f16 v7, v44, v137
	s_nop 0
	v_pk_max_f16 v6, v6, v7
	s_nop 0
	v_cndmask_b32_e64 v7, v1, v6, s[44:45]
	v_mfma_f32_32x32x16_f16 a[32:47], v[38:41], v[122:125], a[208:223]
	v_cndmask_b32_e64 v6, v1, v6, s[46:47]
	v_perm_b32 v76, v6, v7, s20
	v_pk_mul_f16 v6, v49, v136
	v_pk_mul_f16 v7, v45, v137
	v_mfma_f32_32x32x16_f16 a[208:223], v[18:21], v[118:121], a[48:63]
	v_pk_max_f16 v6, v6, v7
	s_nop 0
	v_cndmask_b32_e64 v7, v1, v6, s[48:49]
	v_cndmask_b32_e64 v6, v1, v6, s[50:51]
	v_perm_b32 v77, v6, v7, s20
	v_mfma_f32_32x32x16_f16 a[48:63], v[38:41], v[118:121], a[192:207]
	v_pk_add_f16 v6, v75, v74
	v_pk_add_f16 v7, v76, v77
	s_nop 0
	v_pk_add_f16 v6, v6, v7
	s_nop 0
	v_dot2c_f32_f16_e32 v134, 0x3c003c00, v6
	v_mfma_f32_32x32x16_f16 a[192:207], v[18:21], v[106:109], a[64:79]
	v_pk_mul_f16 v6, v46, v140
	v_pk_mul_f16 v7, v42, v139
	s_nop 0
	v_pk_max_f16 v6, v6, v7
	s_nop 0
	v_cndmask_b32_e64 v7, v138, v6, s[4:5]
	v_mfma_f32_32x32x16_f16 a[64:79], v[38:41], v[106:109], a[176:191]
	v_pk_mul_f16 v8, v47, v140
	v_pk_mul_f16 v9, v43, v139
	v_cndmask_b32_e64 v6, v138, v6, s[6:7]
	v_pk_max_f16 v8, v8, v9
	v_mfma_f32_32x32x16_f16 a[176:191], v[18:21], v[98:101], a[112:127]
	v_pk_mul_f16 v30, v48, v140
	v_pk_mul_f16 v31, v44, v139
	v_cndmask_b32_e64 v9, v138, v8, s[8:9]
	v_cndmask_b32_e64 v8, v138, v8, s[10:11]
	v_mfma_f32_32x32x16_f16 a[112:127], v[38:41], v[98:101], a[160:175]
	v_pk_max_f16 v30, v30, v31
	v_pk_mul_f16 v32, v49, v140
	v_cndmask_b32_e64 v31, v138, v30, s[12:13]
	v_cndmask_b32_e64 v30, v138, v30, s[14:15]
	v_mfma_f32_32x32x16_f16 a[160:175], v[18:21], v[94:97], a[128:143]
	v_pk_mul_f16 v33, v45, v139
	s_nop 0
	v_pk_max_f16 v32, v32, v33
	s_nop 0
	v_cndmask_b32_e64 v33, v138, v32, s[16:17]
	v_cndmask_b32_e64 v32, v138, v32, s[18:19]
	v_mfma_f32_32x32x16_f16 a[128:143], v[38:41], v[94:97], a[144:159]
	v_perm_b32 v78, v6, v7, s20
	v_perm_b32 v79, v8, v9, s20
	v_perm_b32 v80, v30, v31, s20
	v_perm_b32 v81, v32, v33, s20
	v_pk_add_f16 v6, v79, v78
	v_pk_add_f16 v7, v80, v81
	v_accvgpr_write_b32 a80, v160
	v_pk_add_f16 v6, v6, v7
	v_accvgpr_write_b32 a81, v161
	v_accvgpr_write_b32 a82, v162
	v_accvgpr_write_b32 a83, v163
	v_accvgpr_write_b32 a84, v164
	v_accvgpr_write_b32 a85, v165
	v_accvgpr_write_b32 a86, v166
	v_accvgpr_write_b32 a87, v167
	v_accvgpr_write_b32 a88, v168
	v_accvgpr_write_b32 a89, v169
	v_accvgpr_write_b32 a90, v170
	v_accvgpr_write_b32 a91, v171
	v_accvgpr_write_b32 a92, v172
	v_accvgpr_write_b32 a93, v173
	v_accvgpr_write_b32 a94, v174
	v_accvgpr_write_b32 a95, v175
	v_dot2c_f32_f16_e32 v135, 0x3c003c00, v6
	s_nop 0
	v_mfma_f32_32x32x16_f16 a[144:159], v[18:21], v[86:89], a[80:95]
	v_mfma_f32_32x32x16_f16 a[80:95], v[38:41], v[86:89], a[96:111]
	s_nop 6
	v_accvgpr_write_b32 a96, v144
	v_accvgpr_write_b32 a97, v145
	v_accvgpr_write_b32 a98, v146
	v_accvgpr_write_b32 a99, v147
	v_accvgpr_write_b32 a100, v148
	v_accvgpr_write_b32 a101, v149
	v_accvgpr_write_b32 a102, v150
	v_accvgpr_write_b32 a103, v151
	v_accvgpr_write_b32 a104, v152
	v_accvgpr_write_b32 a105, v153
	v_accvgpr_write_b32 a106, v154
	v_accvgpr_write_b32 a107, v155
	v_accvgpr_write_b32 a108, v156
	v_accvgpr_write_b32 a109, v157
	v_accvgpr_write_b32 a110, v158
	v_accvgpr_write_b32 a111, v159
	s_waitcnt lgkmcnt(0)
	s_nop 0
	v_mfma_f32_32x32x16_f16 a[96:111], v[74:77], v[82:85], a[96:111]
	ds_read_b128 v[86:89], v141 offset:64
	ds_read_b128 v[70:73], v141 offset:4672
	ds_read_b128 v[62:65], v141 offset:9280
	ds_read_b128 v[42:45], v141 offset:13888
	ds_read_b128 v[38:41], v141 offset:18496
	ds_read_b128 v[30:33], v141 offset:23104
	ds_read_b128 v[18:21], v141 offset:27712
	ds_read_b128 v[6:9], v141 offset:32320
	s_load_dwordx16 s[36:51], s[0:1], 0xfc0
	s_load_dwordx16 s[4:19], s[0:1], 0x8fc0
	ds_read_b128 v[66:69], v142 offset:2016
	ds_read_b128 v[46:49], v143 offset:2016
	v_mfma_f32_32x32x16_f16 a[0:15], v[78:81], v[82:85], a[0:15]
	v_pk_mul_f16 v82, v54, v136
	v_pk_mul_f16 v83, v34, v137
	s_nop 0
	v_pk_max_f16 v82, v82, v83
	s_nop 0
	v_cndmask_b32_e64 v83, v1, v82, s[68:69]
	v_mfma_f32_32x32x16_f16 a[240:255], v[74:77], v[58:61], a[240:255]
	v_cndmask_b32_e64 v82, v1, v82, s[70:71]
	v_perm_b32 v82, v82, v83, s20
	v_pk_mul_f16 v83, v55, v136
	v_pk_mul_f16 v84, v35, v137
	v_mfma_f32_32x32x16_f16 a[16:31], v[78:81], v[58:61], a[16:31]
	v_pk_max_f16 v58, v83, v84
	s_nop 0
	v_cndmask_b32_e64 v59, v1, v58, s[72:73]
	v_cndmask_b32_e64 v58, v1, v58, s[74:75]
	v_perm_b32 v83, v58, v59, s20
	v_mfma_f32_32x32x16_f16 a[224:239], v[74:77], v[50:53], a[224:239]
	v_pk_mul_f16 v58, v56, v136
	v_pk_mul_f16 v59, v36, v137
	s_nop 0
	v_pk_max_f16 v58, v58, v59
	s_nop 0
	v_cndmask_b32_e64 v59, v1, v58, s[76:77]
	v_mfma_f32_32x32x16_f16 a[32:47], v[78:81], v[50:53], a[32:47]
	v_cndmask_b32_e64 v50, v1, v58, s[78:79]
	v_perm_b32 v84, v50, v59, s20
	v_pk_mul_f16 v50, v57, v136
	v_pk_mul_f16 v51, v37, v137
	v_mfma_f32_32x32x16_f16 a[208:223], v[74:77], v[26:29], a[208:223]
	v_pk_max_f16 v50, v50, v51
	s_nop 0
	v_cndmask_b32_e64 v51, v1, v50, s[80:81]
	v_cndmask_b32_e64 v50, v1, v50, s[82:83]
	v_perm_b32 v85, v50, v51, s20
	v_mfma_f32_32x32x16_f16 a[48:63], v[78:81], v[26:29], a[48:63]
	v_pk_add_f16 v26, v83, v82
	v_pk_add_f16 v27, v84, v85
	s_nop 0
	v_pk_add_f16 v26, v26, v27
	s_nop 0
	v_dot2c_f32_f16_e32 v134, 0x3c003c00, v26
	v_mfma_f32_32x32x16_f16 a[192:207], v[74:77], v[22:25], a[192:207]
	v_pk_mul_f16 v26, v54, v140
	v_pk_mul_f16 v27, v34, v139
	s_nop 0
	v_pk_max_f16 v26, v26, v27
	s_nop 0
	v_cndmask_b32_e64 v27, v138, v26, s[52:53]
	v_mfma_f32_32x32x16_f16 a[64:79], v[78:81], v[22:25], a[64:79]
	v_pk_mul_f16 v23, v55, v140
	v_pk_mul_f16 v24, v35, v139
	v_cndmask_b32_e64 v22, v138, v26, s[54:55]
	v_pk_max_f16 v23, v23, v24
	v_mfma_f32_32x32x16_f16 a[176:191], v[74:77], v[14:17], a[176:191]
	v_pk_mul_f16 v25, v56, v140
	v_pk_mul_f16 v26, v36, v139
	v_cndmask_b32_e64 v24, v138, v23, s[56:57]
	v_cndmask_b32_e64 v23, v138, v23, s[58:59]
	v_mfma_f32_32x32x16_f16 a[112:127], v[78:81], v[14:17], a[112:127]
	v_pk_max_f16 v14, v25, v26
	v_pk_mul_f16 v16, v57, v140
	v_cndmask_b32_e64 v15, v138, v14, s[60:61]
	v_cndmask_b32_e64 v14, v138, v14, s[62:63]
	v_mfma_f32_32x32x16_f16 a[160:175], v[74:77], v[10:13], a[160:175]
	v_pk_mul_f16 v17, v37, v139
	s_nop 0
	v_pk_max_f16 v16, v16, v17
	s_nop 0
	v_cndmask_b32_e64 v17, v138, v16, s[64:65]
	v_cndmask_b32_e64 v16, v138, v16, s[66:67]
	v_mfma_f32_32x32x16_f16 a[128:143], v[78:81], v[10:13], a[128:143]
	v_perm_b32 v10, v22, v27, s20
	v_perm_b32 v11, v23, v24, s20
	v_perm_b32 v12, v14, v15, s20
	v_perm_b32 v13, v16, v17, s20
	v_mfma_f32_32x32x16_f16 a[144:159], v[74:77], v[2:5], a[144:159]
	v_pk_add_f16 v14, v11, v10
	v_pk_add_f16 v15, v12, v13
	s_nop 0
	v_pk_add_f16 v14, v14, v15
	s_nop 0
	v_dot2c_f32_f16_e32 v135, 0x3c003c00, v14
	v_mfma_f32_32x32x16_f16 a[80:95], v[78:81], v[2:5], a[80:95]
	s_waitcnt lgkmcnt(0)
	v_mfma_f32_32x32x16_f16 a[96:111], v[82:85], v[86:89], a[96:111]
	ds_read_b128 v[2:5], v141 offset:96
	ds_read_b128 v[14:17], v141 offset:4704
	ds_read_b128 v[22:25], v141 offset:9312
	ds_read_b128 v[26:29], v141 offset:13920
	ds_read_b128 v[34:37], v141 offset:18528
	ds_read_b128 v[50:53], v141 offset:23136
	ds_read_b128 v[54:57], v141 offset:27744
	ds_read_b128 v[58:61], v141 offset:32352
	v_mfma_f32_32x32x16_f16 a[0:15], v[10:13], v[86:89], a[0:15]
	v_pk_mul_f16 v74, v136, v66
	v_pk_mul_f16 v75, v137, v46
	s_nop 0
	v_pk_max_f16 v74, v74, v75
	s_nop 0
	v_cndmask_b32_e64 v75, v1, v74, s[36:37]
	v_mfma_f32_32x32x16_f16 a[240:255], v[82:85], v[70:73], a[240:255]
	v_cndmask_b32_e64 v74, v1, v74, s[38:39]
	v_perm_b32 v74, v74, v75, s20
	v_pk_mul_f16 v75, v136, v67
	v_pk_mul_f16 v76, v137, v47
	v_mfma_f32_32x32x16_f16 a[16:31], v[10:13], v[70:73], a[16:31]
	v_pk_max_f16 v70, v75, v76
	s_nop 0
	v_cndmask_b32_e64 v71, v1, v70, s[40:41]
	v_cndmask_b32_e64 v70, v1, v70, s[42:43]
	v_perm_b32 v75, v70, v71, s20
	v_mfma_f32_32x32x16_f16 a[224:239], v[82:85], v[62:65], a[224:239]
	v_pk_mul_f16 v70, v136, v68
	v_pk_mul_f16 v71, v137, v48
	s_nop 0
	v_pk_max_f16 v70, v70, v71
	s_nop 0
	v_cndmask_b32_e64 v71, v1, v70, s[44:45]
	v_mfma_f32_32x32x16_f16 a[32:47], v[10:13], v[62:65], a[32:47]
	v_cndmask_b32_e64 v62, v1, v70, s[46:47]
	v_perm_b32 v76, v62, v71, s20
	v_pk_mul_f16 v62, v136, v69
	v_pk_mul_f16 v63, v137, v49
	v_mfma_f32_32x32x16_f16 a[208:223], v[82:85], v[42:45], a[208:223]
	v_pk_max_f16 v62, v62, v63
	s_nop 0
	v_cndmask_b32_e64 v63, v1, v62, s[48:49]
	v_cndmask_b32_e64 v1, v1, v62, s[50:51]
	v_perm_b32 v77, v1, v63, s20
	v_mfma_f32_32x32x16_f16 a[48:63], v[10:13], v[42:45], a[48:63]
	v_pk_add_f16 v1, v75, v74
	v_pk_add_f16 v42, v76, v77
	s_nop 0
	v_pk_add_f16 v1, v1, v42
	s_nop 0
	v_dot2c_f32_f16_e32 v134, 0x3c003c00, v1
	v_mfma_f32_32x32x16_f16 a[192:207], v[82:85], v[38:41], a[192:207]
	v_pk_mul_f16 v1, v140, v66
	v_pk_mul_f16 v42, v139, v46
	s_nop 0
	v_pk_max_f16 v1, v1, v42
	s_nop 0
	v_cndmask_b32_e64 v42, v138, v1, s[4:5]
	v_mfma_f32_32x32x16_f16 a[64:79], v[10:13], v[38:41], a[64:79]
	v_pk_mul_f16 v38, v140, v67
	v_pk_mul_f16 v39, v139, v47
	v_cndmask_b32_e64 v1, v138, v1, s[6:7]
	v_pk_max_f16 v38, v38, v39
	v_mfma_f32_32x32x16_f16 a[176:191], v[82:85], v[30:33], a[176:191]
	v_pk_mul_f16 v40, v140, v68
	v_pk_mul_f16 v41, v139, v48
	v_cndmask_b32_e64 v39, v138, v38, s[8:9]
	v_cndmask_b32_e64 v38, v138, v38, s[10:11]
	v_mfma_f32_32x32x16_f16 a[112:127], v[10:13], v[30:33], a[112:127]
	v_pk_max_f16 v30, v40, v41
	v_pk_mul_f16 v32, v140, v69
	v_cndmask_b32_e64 v31, v138, v30, s[12:13]
	v_cndmask_b32_e64 v30, v138, v30, s[14:15]
	v_mfma_f32_32x32x16_f16 a[160:175], v[82:85], v[18:21], a[160:175]
	v_pk_mul_f16 v33, v139, v49
	s_nop 0
	v_pk_max_f16 v32, v32, v33
	s_nop 0
	v_cndmask_b32_e64 v33, v138, v32, s[16:17]
	v_cndmask_b32_e64 v32, v138, v32, s[18:19]
	v_mfma_f32_32x32x16_f16 a[128:143], v[10:13], v[18:21], a[128:143]
	v_perm_b32 v18, v1, v42, s20
	v_perm_b32 v19, v38, v39, s20
	v_perm_b32 v20, v30, v31, s20
	v_perm_b32 v21, v32, v33, s20
	v_mfma_f32_32x32x16_f16 a[144:159], v[82:85], v[6:9], a[144:159]
	v_pk_add_f16 v1, v19, v18
	v_pk_add_f16 v30, v20, v21
	s_nop 0
	v_pk_add_f16 v1, v1, v30
	s_nop 0
	v_dot2c_f32_f16_e32 v135, 0x3c003c00, v1
	v_mfma_f32_32x32x16_f16 a[80:95], v[10:13], v[6:9], a[80:95]
	s_waitcnt lgkmcnt(7)
	v_mfma_f32_32x32x16_f16 a[96:111], v[74:77], v[2:5], a[96:111]
	v_mfma_f32_32x32x16_f16 a[0:15], v[18:21], v[2:5], a[0:15]
	s_waitcnt lgkmcnt(6)
	v_mfma_f32_32x32x16_f16 a[240:255], v[74:77], v[14:17], a[240:255]
	v_mfma_f32_32x32x16_f16 a[16:31], v[18:21], v[14:17], a[16:31]
	s_waitcnt lgkmcnt(5)
	v_mfma_f32_32x32x16_f16 a[224:239], v[74:77], v[22:25], a[224:239]
	v_mfma_f32_32x32x16_f16 a[32:47], v[18:21], v[22:25], a[32:47]
	s_waitcnt lgkmcnt(4)
	v_mfma_f32_32x32x16_f16 a[208:223], v[74:77], v[26:29], a[208:223]
	v_mfma_f32_32x32x16_f16 a[48:63], v[18:21], v[26:29], a[48:63]
	s_waitcnt lgkmcnt(3)
	v_mfma_f32_32x32x16_f16 a[192:207], v[74:77], v[34:37], a[192:207]
	v_mfma_f32_32x32x16_f16 a[64:79], v[18:21], v[34:37], a[64:79]
	s_waitcnt lgkmcnt(2)
	v_mfma_f32_32x32x16_f16 a[176:191], v[74:77], v[50:53], a[176:191]
	v_mfma_f32_32x32x16_f16 a[112:127], v[18:21], v[50:53], a[112:127]
	s_waitcnt lgkmcnt(1)
	v_mfma_f32_32x32x16_f16 a[160:175], v[74:77], v[54:57], a[160:175]
	v_mfma_f32_32x32x16_f16 a[128:143], v[18:21], v[54:57], a[128:143]
	s_waitcnt lgkmcnt(0)
	v_mfma_f32_32x32x16_f16 a[144:159], v[74:77], v[58:61], a[144:159]
	v_mfma_f32_32x32x16_f16 a[80:95], v[18:21], v[58:61], a[80:95]
	v_readfirstlane_b32 s1, v0
	s_and_b32 s0, s3, 0xffffff00
	s_andn2_b32 s1, s1, 63
	s_add_i32 s4, s1, s0
	s_lshl_b32 s0, s2, 13
	s_and_b32 s6, s0, 0xe000
	s_ashr_i32 s5, s4, 31
	s_add_u32 s0, s4, s6
	s_addc_u32 s1, s5, 0
	s_lshl_b64 s[2:3], s[0:1], 9
	v_lshrrev_b32_e32 v0, 3, v132
	s_add_u32 s2, s22, s2
	v_and_b32_e32 v3, 12, v0
	s_addc_u32 s3, s23, s3
	v_lshlrev_b32_e32 v0, 9, v3
	v_mov_b32_e32 v1, 0
	v_lshl_add_u64 v[4:5], s[2:3], 0, v[0:1]
	v_lshlrev_b32_e32 v0, 4, v132
	v_and_b32_e32 v0, 0x1f0, v0
	v_lshl_add_u64 v[4:5], v[4:5], 0, v[0:1]
	v_accvgpr_read_b32 v6, a96
	v_accvgpr_read_b32 v7, a240
	v_accvgpr_read_b32 v8, a224
	v_max3_f32 v0, |v6|, |v7|, |v8|
	v_accvgpr_read_b32 v9, a208
	v_accvgpr_read_b32 v14, a192
	v_max3_f32 v0, |v0|, |v9|, |v14|
	v_accvgpr_read_b32 v15, a176
	v_accvgpr_read_b32 v16, a160
	v_max3_f32 v0, |v0|, |v15|, |v16|
	v_accvgpr_read_b32 v10, a144
	v_accvgpr_read_b32 v17, a144
	v_max3_f32 v10, |v0|, |v17|, |v10|
	v_accvgpr_read_b32 v18, a97
	v_accvgpr_read_b32 v19, a241
	v_accvgpr_read_b32 v20, a225
	v_max3_f32 v0, |v18|, |v19|, |v20|
	v_accvgpr_read_b32 v21, a209
	v_accvgpr_read_b32 v22, a193
	v_max3_f32 v0, |v0|, |v21|, |v22|
	v_accvgpr_read_b32 v23, a177
	v_accvgpr_read_b32 v24, a161
	v_max3_f32 v0, |v0|, |v23|, |v24|
	v_accvgpr_read_b32 v11, a145
	v_accvgpr_read_b32 v25, a145
	v_max3_f32 v11, |v0|, |v25|, |v11|
	v_accvgpr_read_b32 v26, a98
	v_accvgpr_read_b32 v27, a242
	v_accvgpr_read_b32 v28, a226
	v_max3_f32 v0, |v26|, |v27|, |v28|
	v_accvgpr_read_b32 v29, a210
	v_accvgpr_read_b32 v30, a194
	v_max3_f32 v0, |v0|, |v29|, |v30|
	v_accvgpr_read_b32 v31, a178
	v_accvgpr_read_b32 v32, a162
	v_max3_f32 v0, |v0|, |v31|, |v32|
	v_accvgpr_read_b32 v12, a146
	v_accvgpr_read_b32 v33, a146
	v_max3_f32 v12, |v0|, |v33|, |v12|
	v_accvgpr_read_b32 v34, a99
	v_accvgpr_read_b32 v35, a243
	v_accvgpr_read_b32 v36, a227
	v_max3_f32 v0, |v34|, |v35|, |v36|
	v_accvgpr_read_b32 v37, a211
	v_accvgpr_read_b32 v38, a195
	v_max3_f32 v0, |v0|, |v37|, |v38|
	v_accvgpr_read_b32 v13, a147
	v_accvgpr_read_b32 v39, a179
	v_accvgpr_read_b32 v40, a163
	v_max3_f32 v0, |v0|, |v39|, |v40|
	v_accvgpr_read_b32 v41, a147
	v_max3_f32 v13, |v0|, |v41|, |v13|
	v_lshlrev_b32_e32 v0, 2, v3
	s_nop 1
	v_max_f32_dpp v10, v10, v10 quad_perm:[1,0,3,2] row_mask:0xf bank_mask:0xf
	v_max_f32_dpp v11, v11, v11 quad_perm:[1,0,3,2] row_mask:0xf bank_mask:0xf
	v_max_f32_dpp v12, v12, v12 quad_perm:[1,0,3,2] row_mask:0xf bank_mask:0xf
	v_max_f32_dpp v13, v13, v13 quad_perm:[1,0,3,2] row_mask:0xf bank_mask:0xf
	v_max_f32_dpp v10, v10, v10 quad_perm:[2,3,0,1] row_mask:0xf bank_mask:0xf
	v_max_f32_dpp v11, v11, v11 quad_perm:[2,3,0,1] row_mask:0xf bank_mask:0xf
	v_max_f32_dpp v12, v12, v12 quad_perm:[2,3,0,1] row_mask:0xf bank_mask:0xf
	v_max_f32_dpp v13, v13, v13 quad_perm:[2,3,0,1] row_mask:0xf bank_mask:0xf
	v_max_f32_dpp v10, v10, v10 row_half_mirror row_mask:0xf bank_mask:0xf
	v_max_f32_dpp v11, v11, v11 row_half_mirror row_mask:0xf bank_mask:0xf
	v_max_f32_dpp v12, v12, v12 row_half_mirror row_mask:0xf bank_mask:0xf
	v_max_f32_dpp v13, v13, v13 row_half_mirror row_mask:0xf bank_mask:0xf
	v_max_f32_dpp v10, v10, v10 row_mirror row_mask:0xf bank_mask:0xf
	v_max_f32_dpp v11, v11, v11 row_mirror row_mask:0xf bank_mask:0xf
	v_max_f32_dpp v12, v12, v12 row_mirror row_mask:0xf bank_mask:0xf
	v_max_f32_dpp v13, v13, v13 row_mirror row_mask:0xf bank_mask:0xf
	s_nop 0
	ds_swizzle_b32 v232, v10 offset:swizzle(SWAP,16)
	ds_swizzle_b32 v233, v12 offset:swizzle(SWAP,16)
	ds_swizzle_b32 v234, v11 offset:swizzle(SWAP,16)
	ds_swizzle_b32 v235, v13 offset:swizzle(SWAP,16)
	s_waitcnt lgkmcnt(0)
	v_max_f32_e32 v10, v10, v232
	v_rcp_f32_e32 v42, v10
	v_cmp_lt_f32_e32 vcc, 0, v10
	s_waitcnt lgkmcnt(0)
	v_max_f32_e32 v12, v12, v233
	s_waitcnt lgkmcnt(0)
	v_max_f32_e32 v11, v11, v234
	s_lshl_b32 s2, s6, 2
	v_cndmask_b32_e32 v3, 0, v42, vcc
	v_pk_mul_f32 v[224:225], v[6:7], v[2:3] op_sel:[0,1] op_sel_hi:[1,1]
	v_pk_mul_f32 v[226:227], v[8:9], v[2:3] op_sel:[0,1] op_sel_hi:[1,1]
	v_cvt_pknorm_i16_f32 v6, v224, v225
	v_cvt_pknorm_i16_f32 v7, v226, v227
	v_pk_mul_f32 v[228:229], v[14:15], v[2:3] op_sel:[0,1] op_sel_hi:[1,1]
	v_rcp_f32_e32 v14, v11
	v_cvt_pknorm_i16_f32 v8, v228, v229
	v_pk_mul_f32 v[230:231], v[16:17], v[2:3] op_sel:[0,1] op_sel_hi:[1,1]
	v_cmp_lt_f32_e32 vcc, 0, v11
	v_cvt_pknorm_i16_f32 v9, v230, v231
	global_store_dwordx4 v[4:5], v[6:9], off sc0 sc1
	s_nop 1
	s_add_u32 s6, s24, s2
	v_cndmask_b32_e32 v3, 0, v14, vcc
	v_pk_mul_f32 v[224:225], v[18:19], v[2:3] op_sel:[0,1] op_sel_hi:[1,1]
	v_pk_mul_f32 v[226:227], v[20:21], v[2:3] op_sel:[0,1] op_sel_hi:[1,1]
	v_cvt_pknorm_i16_f32 v6, v224, v225
	v_cvt_pknorm_i16_f32 v7, v226, v227
	v_pk_mul_f32 v[228:229], v[22:23], v[2:3] op_sel:[0,1] op_sel_hi:[1,1]
	v_pk_mul_f32 v[230:231], v[24:25], v[2:3] op_sel:[0,1] op_sel_hi:[1,1]
	v_cvt_pknorm_i16_f32 v8, v228, v229
	v_cvt_pknorm_i16_f32 v9, v230, v231
	v_rcp_f32_e32 v3, v12
	s_addc_u32 s7, s25, 0
	s_lshl_b64 s[2:3], s[4:5], 2
	s_mov_b64 s[4:5], 0x200
	s_add_u32 s2, s6, s2
	v_lshl_add_u64 v[14:15], v[4:5], 0, s[4:5]
	s_mov_b32 s4, 0x38000100
	v_cmp_lt_f32_e32 vcc, 0, v12
	s_addc_u32 s3, s7, s3
	global_store_dwordx4 v[14:15], v[6:9], off sc0 sc1
	s_nop 1
	v_pk_mul_f32 v[6:7], v[10:11], s[4:5] op_sel_hi:[1,0]
	v_cndmask_b32_e32 v3, 0, v3, vcc
	global_store_dwordx2 v0, v[6:7], s[2:3]
	v_pk_mul_f32 v[224:225], v[26:27], v[2:3] op_sel:[0,1] op_sel_hi:[1,1]
	v_pk_mul_f32 v[226:227], v[28:29], v[2:3] op_sel:[0,1] op_sel_hi:[1,1]
	v_cvt_pknorm_i16_f32 v6, v224, v225
	v_cvt_pknorm_i16_f32 v7, v226, v227
	v_pk_mul_f32 v[228:229], v[30:31], v[2:3] op_sel:[0,1] op_sel_hi:[1,1]
	v_pk_mul_f32 v[230:231], v[32:33], v[2:3] op_sel:[0,1] op_sel_hi:[1,1]
	v_cvt_pknorm_i16_f32 v8, v228, v229
	s_waitcnt lgkmcnt(0)
	v_max_f32_e32 v13, v13, v235
	v_cvt_pknorm_i16_f32 v9, v230, v231
	v_rcp_f32_e32 v3, v13
	v_cmp_lt_f32_e32 vcc, 0, v13
	s_mov_b64 s[6:7], 0x400
	v_lshl_add_u64 v[10:11], v[4:5], 0, s[6:7]
	v_cndmask_b32_e32 v3, 0, v3, vcc
	global_store_dwordx4 v[10:11], v[6:9], off sc0 sc1
	s_nop 1
	v_pk_mul_f32 v[224:225], v[34:35], v[2:3] op_sel:[0,1] op_sel_hi:[1,1]
	v_pk_mul_f32 v[226:227], v[36:37], v[2:3] op_sel:[0,1] op_sel_hi:[1,1]
	v_cvt_pknorm_i16_f32 v6, v224, v225
	v_cvt_pknorm_i16_f32 v7, v226, v227
	v_pk_mul_f32 v[228:229], v[38:39], v[2:3] op_sel:[0,1] op_sel_hi:[1,1]
	v_pk_mul_f32 v[230:231], v[40:41], v[2:3] op_sel:[0,1] op_sel_hi:[1,1]
	v_cvt_pknorm_i16_f32 v8, v228, v229
	s_mov_b64 s[6:7], 0x600
	v_cvt_pknorm_i16_f32 v9, v230, v231
	v_lshl_add_u64 v[10:11], v[4:5], 0, s[6:7]
	global_store_dwordx4 v[10:11], v[6:9], off sc0 sc1
	s_nop 1
	v_pk_mul_f32 v[6:7], v[12:13], s[4:5] op_sel_hi:[1,0]
	v_lshlrev_b32_e32 v2, 2, v132
	global_store_dwordx2 v0, v[6:7], s[2:3] offset:8
	v_accvgpr_read_b32 v42, a100
	v_accvgpr_read_b32 v6, a244
	v_accvgpr_read_b32 v7, a228
	v_max3_f32 v8, |v42|, |v6|, |v7|
	v_accvgpr_read_b32 v9, a212
	v_accvgpr_read_b32 v14, a196
	v_max3_f32 v8, |v8|, |v9|, |v14|
	v_accvgpr_read_b32 v15, a180
	v_accvgpr_read_b32 v16, a164
	v_max3_f32 v8, |v8|, |v15|, |v16|
	v_accvgpr_read_b32 v10, a148
	v_accvgpr_read_b32 v43, a101
	v_accvgpr_read_b32 v17, a148
	v_max3_f32 v8, |v8|, |v17|, |v10|
	v_accvgpr_read_b32 v19, a245
	v_accvgpr_read_b32 v20, a229
	v_max3_f32 v10, |v43|, |v19|, |v20|
	v_accvgpr_read_b32 v21, a213
	v_accvgpr_read_b32 v22, a197
	v_max3_f32 v10, |v10|, |v21|, |v22|
	v_accvgpr_read_b32 v23, a181
	v_accvgpr_read_b32 v24, a165
	v_max3_f32 v10, |v10|, |v23|, |v24|
	v_accvgpr_read_b32 v11, a149
	v_accvgpr_read_b32 v44, a102
	v_accvgpr_read_b32 v25, a149
	v_max3_f32 v11, |v10|, |v25|, |v11|
	v_accvgpr_read_b32 v27, a246
	v_accvgpr_read_b32 v28, a230
	v_max3_f32 v10, |v44|, |v27|, |v28|
	v_accvgpr_read_b32 v29, a214
	v_accvgpr_read_b32 v30, a198
	v_max3_f32 v10, |v10|, |v29|, |v30|
	v_accvgpr_read_b32 v31, a182
	v_accvgpr_read_b32 v32, a166
	v_max3_f32 v10, |v10|, |v31|, |v32|
	v_accvgpr_read_b32 v12, a150
	v_accvgpr_read_b32 v45, a103
	v_accvgpr_read_b32 v33, a150
	v_max3_f32 v12, |v10|, |v33|, |v12|
	v_accvgpr_read_b32 v35, a247
	v_accvgpr_read_b32 v36, a231
	v_max3_f32 v10, |v45|, |v35|, |v36|
	v_accvgpr_read_b32 v37, a215
	v_accvgpr_read_b32 v38, a199
	v_max3_f32 v10, |v10|, |v37|, |v38|
	v_accvgpr_read_b32 v13, a151
	v_accvgpr_read_b32 v39, a183
	v_accvgpr_read_b32 v40, a167
	v_max3_f32 v10, |v10|, |v39|, |v40|
	v_accvgpr_read_b32 v41, a151
	v_max3_f32 v13, |v10|, |v41|, |v13|
	v_mov_b32_e32 v3, v42
	s_nop 1
	v_max_f32_dpp v8, v8, v8 quad_perm:[1,0,3,2] row_mask:0xf bank_mask:0xf
	v_max_f32_dpp v11, v11, v11 quad_perm:[1,0,3,2] row_mask:0xf bank_mask:0xf
	v_max_f32_dpp v12, v12, v12 quad_perm:[1,0,3,2] row_mask:0xf bank_mask:0xf
	v_max_f32_dpp v13, v13, v13 quad_perm:[1,0,3,2] row_mask:0xf bank_mask:0xf
	v_max_f32_dpp v8, v8, v8 quad_perm:[2,3,0,1] row_mask:0xf bank_mask:0xf
	v_max_f32_dpp v11, v11, v11 quad_perm:[2,3,0,1] row_mask:0xf bank_mask:0xf
	v_max_f32_dpp v12, v12, v12 quad_perm:[2,3,0,1] row_mask:0xf bank_mask:0xf
	v_max_f32_dpp v13, v13, v13 quad_perm:[2,3,0,1] row_mask:0xf bank_mask:0xf
	v_max_f32_dpp v8, v8, v8 row_half_mirror row_mask:0xf bank_mask:0xf
	v_max_f32_dpp v11, v11, v11 row_half_mirror row_mask:0xf bank_mask:0xf
	v_max_f32_dpp v12, v12, v12 row_half_mirror row_mask:0xf bank_mask:0xf
	v_max_f32_dpp v13, v13, v13 row_half_mirror row_mask:0xf bank_mask:0xf
	v_max_f32_dpp v8, v8, v8 row_mirror row_mask:0xf bank_mask:0xf
	v_max_f32_dpp v11, v11, v11 row_mirror row_mask:0xf bank_mask:0xf
	v_max_f32_dpp v12, v12, v12 row_mirror row_mask:0xf bank_mask:0xf
	v_max_f32_dpp v13, v13, v13 row_mirror row_mask:0xf bank_mask:0xf
	s_nop 0
	ds_swizzle_b32 v232, v8 offset:swizzle(SWAP,16)
	ds_swizzle_b32 v233, v11 offset:swizzle(SWAP,16)
	ds_swizzle_b32 v234, v12 offset:swizzle(SWAP,16)
	ds_swizzle_b32 v235, v13 offset:swizzle(SWAP,16)
	s_waitcnt lgkmcnt(0)
	v_max_f32_e32 v10, v8, v232
	v_rcp_f32_e32 v8, v10
	v_cmp_lt_f32_e32 vcc, 0, v10
	s_waitcnt lgkmcnt(0)
	v_max_f32_e32 v11, v11, v233
	v_mov_b32_e32 v18, v43
	s_mov_b64 s[6:7], 0x1000
	v_cndmask_b32_e32 v42, 0, v8, vcc
	v_mul_f32_e32 v3, v42, v3
	v_mul_f32_e32 v6, v42, v6
	v_cvt_pknorm_i16_f32 v6, v3, v6
	v_mul_f32_e32 v3, v42, v7
	v_mul_f32_e32 v7, v42, v9
	v_cvt_pknorm_i16_f32 v7, v3, v7
	v_pk_mul_f32 v[224:225], v[14:15], v[42:43] op_sel_hi:[1,0]
	v_pk_mul_f32 v[226:227], v[16:17], v[42:43] op_sel_hi:[1,0]
	v_cvt_pknorm_i16_f32 v8, v224, v225
	v_cvt_pknorm_i16_f32 v9, v226, v227
	v_rcp_f32_e32 v3, v11
	v_cmp_lt_f32_e32 vcc, 0, v11
	v_lshl_add_u64 v[14:15], v[4:5], 0, s[6:7]
	global_store_dwordx4 v[14:15], v[6:9], off sc0 sc1
	s_nop 1
	v_cndmask_b32_e32 v3, 0, v3, vcc
	v_pk_mul_f32 v[228:229], v[18:19], v[2:3] op_sel:[0,1] op_sel_hi:[1,1]
	v_pk_mul_f32 v[230:231], v[20:21], v[2:3] op_sel:[0,1] op_sel_hi:[1,1]
	v_cvt_pknorm_i16_f32 v6, v228, v229
	v_cvt_pknorm_i16_f32 v7, v230, v231
	v_pk_mul_f32 v[224:225], v[22:23], v[2:3] op_sel:[0,1] op_sel_hi:[1,1]
	v_pk_mul_f32 v[226:227], v[24:25], v[2:3] op_sel:[0,1] op_sel_hi:[1,1]
	v_cvt_pknorm_i16_f32 v8, v224, v225
	s_waitcnt lgkmcnt(0)
	v_max_f32_e32 v12, v12, v234
	v_cvt_pknorm_i16_f32 v9, v226, v227
	v_rcp_f32_e32 v3, v12
	s_mov_b64 s[6:7], 0x1200
	v_cmp_lt_f32_e32 vcc, 0, v12
	v_mov_b32_e32 v26, v44
	v_lshl_add_u64 v[14:15], v[4:5], 0, s[6:7]
	global_store_dwordx4 v[14:15], v[6:9], off sc0 sc1
	s_nop 1
	v_pk_mul_f32 v[6:7], v[10:11], s[4:5] op_sel_hi:[1,0]
	v_cndmask_b32_e32 v3, 0, v3, vcc
	global_store_dwordx2 v0, v[6:7], s[2:3] offset:32
	v_pk_mul_f32 v[228:229], v[26:27], v[2:3] op_sel:[0,1] op_sel_hi:[1,1]
	v_pk_mul_f32 v[230:231], v[28:29], v[2:3] op_sel:[0,1] op_sel_hi:[1,1]
	v_cvt_pknorm_i16_f32 v6, v228, v229
	v_cvt_pknorm_i16_f32 v7, v230, v231
	v_pk_mul_f32 v[224:225], v[30:31], v[2:3] op_sel:[0,1] op_sel_hi:[1,1]
	v_pk_mul_f32 v[226:227], v[32:33], v[2:3] op_sel:[0,1] op_sel_hi:[1,1]
	v_cvt_pknorm_i16_f32 v8, v224, v225
	s_waitcnt lgkmcnt(0)
	v_max_f32_e32 v13, v13, v235
	v_cvt_pknorm_i16_f32 v9, v226, v227
	v_rcp_f32_e32 v3, v13
	v_cmp_lt_f32_e32 vcc, 0, v13
	v_mov_b32_e32 v34, v45
	s_mov_b64 s[6:7], 0x1400
	v_cndmask_b32_e32 v3, 0, v3, vcc
	v_lshl_add_u64 v[10:11], v[4:5], 0, s[6:7]
	global_store_dwordx4 v[10:11], v[6:9], off sc0 sc1
	s_nop 1
	v_pk_mul_f32 v[228:229], v[34:35], v[2:3] op_sel:[0,1] op_sel_hi:[1,1]
	v_pk_mul_f32 v[230:231], v[36:37], v[2:3] op_sel:[0,1] op_sel_hi:[1,1]
	v_cvt_pknorm_i16_f32 v6, v228, v229
	v_cvt_pknorm_i16_f32 v7, v230, v231
	v_pk_mul_f32 v[224:225], v[38:39], v[2:3] op_sel:[0,1] op_sel_hi:[1,1]
	v_pk_mul_f32 v[226:227], v[40:41], v[2:3] op_sel:[0,1] op_sel_hi:[1,1]
	v_cvt_pknorm_i16_f32 v8, v224, v225
	s_mov_b64 s[6:7], 0x1600
	v_cvt_pknorm_i16_f32 v9, v226, v227
	v_lshl_add_u64 v[10:11], v[4:5], 0, s[6:7]
	global_store_dwordx4 v[10:11], v[6:9], off sc0 sc1
	s_nop 1
	v_pk_mul_f32 v[6:7], v[12:13], s[4:5] op_sel_hi:[1,0]
	v_accvgpr_read_b32 v46, a104
	v_accvgpr_read_b32 v47, a105
	v_accvgpr_read_b32 v48, a106
	v_accvgpr_read_b32 v49, a107
	v_accvgpr_read_b32 v50, a108
	v_accvgpr_read_b32 v51, a109
	v_accvgpr_read_b32 v52, a110
	v_accvgpr_read_b32 v53, a111
	global_store_dwordx2 v0, v[6:7], s[2:3] offset:40
	v_mov_b64_e32 v[42:43], v[46:47]
	v_accvgpr_read_b32 v6, a248
	v_accvgpr_read_b32 v7, a232
	v_max3_f32 v8, |v42|, |v6|, |v7|
	v_accvgpr_read_b32 v9, a216
	v_accvgpr_read_b32 v14, a200
	v_max3_f32 v8, |v8|, |v9|, |v14|
	v_accvgpr_read_b32 v15, a184
	v_accvgpr_read_b32 v16, a168
	v_max3_f32 v8, |v8|, |v15|, |v16|
	v_accvgpr_read_b32 v10, a152
	v_accvgpr_read_b32 v17, a152
	v_max3_f32 v8, |v8|, |v17|, |v10|
	v_accvgpr_read_b32 v19, a249
	v_accvgpr_read_b32 v20, a233
	v_max3_f32 v10, |v43|, |v19|, |v20|
	v_accvgpr_read_b32 v21, a217
	v_accvgpr_read_b32 v22, a201
	v_max3_f32 v10, |v10|, |v21|, |v22|
	v_accvgpr_read_b32 v23, a185
	v_accvgpr_read_b32 v24, a169
	v_max3_f32 v10, |v10|, |v23|, |v24|
	v_accvgpr_read_b32 v11, a153
	v_mov_b64_e32 v[44:45], v[48:49]
	v_accvgpr_read_b32 v25, a153
	v_max3_f32 v11, |v10|, |v25|, |v11|
	v_accvgpr_read_b32 v27, a250
	v_accvgpr_read_b32 v28, a234
	v_max3_f32 v10, |v44|, |v27|, |v28|
	v_accvgpr_read_b32 v29, a218
	v_accvgpr_read_b32 v30, a202
	v_max3_f32 v10, |v10|, |v29|, |v30|
	v_accvgpr_read_b32 v31, a186
	v_accvgpr_read_b32 v32, a170
	v_max3_f32 v10, |v10|, |v31|, |v32|
	v_accvgpr_read_b32 v12, a154
	v_accvgpr_read_b32 v33, a154
	v_max3_f32 v12, |v10|, |v33|, |v12|
	v_accvgpr_read_b32 v35, a251
	v_accvgpr_read_b32 v36, a235
	v_max3_f32 v10, |v45|, |v35|, |v36|
	v_accvgpr_read_b32 v37, a219
	v_accvgpr_read_b32 v38, a203
	v_max3_f32 v10, |v10|, |v37|, |v38|
	v_accvgpr_read_b32 v13, a155
	v_accvgpr_read_b32 v39, a187
	v_accvgpr_read_b32 v40, a171
	v_max3_f32 v10, |v10|, |v39|, |v40|
	v_accvgpr_read_b32 v41, a155
	v_max3_f32 v13, |v10|, |v41|, |v13|
	v_mov_b32_e32 v3, v42
	s_nop 1
	v_max_f32_dpp v8, v8, v8 quad_perm:[1,0,3,2] row_mask:0xf bank_mask:0xf
	v_max_f32_dpp v11, v11, v11 quad_perm:[1,0,3,2] row_mask:0xf bank_mask:0xf
	v_max_f32_dpp v12, v12, v12 quad_perm:[1,0,3,2] row_mask:0xf bank_mask:0xf
	v_max_f32_dpp v13, v13, v13 quad_perm:[1,0,3,2] row_mask:0xf bank_mask:0xf
	v_max_f32_dpp v8, v8, v8 quad_perm:[2,3,0,1] row_mask:0xf bank_mask:0xf
	v_max_f32_dpp v11, v11, v11 quad_perm:[2,3,0,1] row_mask:0xf bank_mask:0xf
	v_max_f32_dpp v12, v12, v12 quad_perm:[2,3,0,1] row_mask:0xf bank_mask:0xf
	v_max_f32_dpp v13, v13, v13 quad_perm:[2,3,0,1] row_mask:0xf bank_mask:0xf
	v_max_f32_dpp v8, v8, v8 row_half_mirror row_mask:0xf bank_mask:0xf
	v_max_f32_dpp v11, v11, v11 row_half_mirror row_mask:0xf bank_mask:0xf
	v_max_f32_dpp v12, v12, v12 row_half_mirror row_mask:0xf bank_mask:0xf
	v_max_f32_dpp v13, v13, v13 row_half_mirror row_mask:0xf bank_mask:0xf
	v_max_f32_dpp v8, v8, v8 row_mirror row_mask:0xf bank_mask:0xf
	v_max_f32_dpp v11, v11, v11 row_mirror row_mask:0xf bank_mask:0xf
	v_max_f32_dpp v12, v12, v12 row_mirror row_mask:0xf bank_mask:0xf
	v_max_f32_dpp v13, v13, v13 row_mirror row_mask:0xf bank_mask:0xf
	s_nop 0
	ds_swizzle_b32 v232, v8 offset:swizzle(SWAP,16)
	ds_swizzle_b32 v233, v11 offset:swizzle(SWAP,16)
	ds_swizzle_b32 v234, v12 offset:swizzle(SWAP,16)
	ds_swizzle_b32 v235, v13 offset:swizzle(SWAP,16)
	s_waitcnt lgkmcnt(0)
	v_max_f32_e32 v10, v8, v232
	v_rcp_f32_e32 v8, v10
	v_cmp_lt_f32_e32 vcc, 0, v10
	s_waitcnt lgkmcnt(0)
	v_max_f32_e32 v11, v11, v233
	v_mov_b32_e32 v18, v43
	s_mov_b64 s[6:7], 0x2000
	v_cndmask_b32_e32 v42, 0, v8, vcc
	v_mul_f32_e32 v3, v42, v3
	v_mul_f32_e32 v6, v42, v6
	v_cvt_pknorm_i16_f32 v6, v3, v6
	v_mul_f32_e32 v3, v42, v7
	v_mul_f32_e32 v7, v42, v9
	v_cvt_pknorm_i16_f32 v7, v3, v7
	v_pk_mul_f32 v[228:229], v[14:15], v[42:43] op_sel_hi:[1,0]
	v_pk_mul_f32 v[230:231], v[16:17], v[42:43] op_sel_hi:[1,0]
	v_cvt_pknorm_i16_f32 v8, v228, v229
	v_cvt_pknorm_i16_f32 v9, v230, v231
	v_rcp_f32_e32 v3, v11
	v_cmp_lt_f32_e32 vcc, 0, v11
	v_lshl_add_u64 v[14:15], v[4:5], 0, s[6:7]
	global_store_dwordx4 v[14:15], v[6:9], off sc0 sc1
	s_nop 1
	v_cndmask_b32_e32 v3, 0, v3, vcc
	v_pk_mul_f32 v[224:225], v[18:19], v[2:3] op_sel:[0,1] op_sel_hi:[1,1]
	v_pk_mul_f32 v[226:227], v[20:21], v[2:3] op_sel:[0,1] op_sel_hi:[1,1]
	v_cvt_pknorm_i16_f32 v6, v224, v225
	v_cvt_pknorm_i16_f32 v7, v226, v227
	v_pk_mul_f32 v[228:229], v[22:23], v[2:3] op_sel:[0,1] op_sel_hi:[1,1]
	v_pk_mul_f32 v[230:231], v[24:25], v[2:3] op_sel:[0,1] op_sel_hi:[1,1]
	v_cvt_pknorm_i16_f32 v8, v228, v229
	s_waitcnt lgkmcnt(0)
	v_max_f32_e32 v12, v12, v234
	v_cvt_pknorm_i16_f32 v9, v230, v231
	v_rcp_f32_e32 v3, v12
	s_mov_b64 s[6:7], 0x2200
	v_cmp_lt_f32_e32 vcc, 0, v12
	v_mov_b32_e32 v26, v44
	v_lshl_add_u64 v[14:15], v[4:5], 0, s[6:7]
	global_store_dwordx4 v[14:15], v[6:9], off sc0 sc1
	s_nop 1
	v_pk_mul_f32 v[6:7], v[10:11], s[4:5] op_sel_hi:[1,0]
	v_cndmask_b32_e32 v3, 0, v3, vcc
	global_store_dwordx2 v0, v[6:7], s[2:3] offset:64
	v_pk_mul_f32 v[224:225], v[26:27], v[2:3] op_sel:[0,1] op_sel_hi:[1,1]
	v_pk_mul_f32 v[226:227], v[28:29], v[2:3] op_sel:[0,1] op_sel_hi:[1,1]
	v_cvt_pknorm_i16_f32 v6, v224, v225
	v_cvt_pknorm_i16_f32 v7, v226, v227
	v_pk_mul_f32 v[228:229], v[30:31], v[2:3] op_sel:[0,1] op_sel_hi:[1,1]
	v_pk_mul_f32 v[230:231], v[32:33], v[2:3] op_sel:[0,1] op_sel_hi:[1,1]
	v_cvt_pknorm_i16_f32 v8, v228, v229
	s_waitcnt lgkmcnt(0)
	v_max_f32_e32 v13, v13, v235
	v_cvt_pknorm_i16_f32 v9, v230, v231
	v_rcp_f32_e32 v3, v13
	v_cmp_lt_f32_e32 vcc, 0, v13
	v_mov_b32_e32 v34, v45
	s_mov_b64 s[6:7], 0x2400
	v_cndmask_b32_e32 v3, 0, v3, vcc
	v_lshl_add_u64 v[10:11], v[4:5], 0, s[6:7]
	global_store_dwordx4 v[10:11], v[6:9], off sc0 sc1
	s_nop 1
	v_pk_mul_f32 v[224:225], v[34:35], v[2:3] op_sel:[0,1] op_sel_hi:[1,1]
	v_pk_mul_f32 v[226:227], v[36:37], v[2:3] op_sel:[0,1] op_sel_hi:[1,1]
	v_cvt_pknorm_i16_f32 v6, v224, v225
	v_cvt_pknorm_i16_f32 v7, v226, v227
	v_pk_mul_f32 v[228:229], v[38:39], v[2:3] op_sel:[0,1] op_sel_hi:[1,1]
	v_pk_mul_f32 v[230:231], v[40:41], v[2:3] op_sel:[0,1] op_sel_hi:[1,1]
	v_cvt_pknorm_i16_f32 v8, v228, v229
	s_mov_b64 s[6:7], 0x2600
	v_cvt_pknorm_i16_f32 v9, v230, v231
	v_lshl_add_u64 v[10:11], v[4:5], 0, s[6:7]
	global_store_dwordx4 v[10:11], v[6:9], off sc0 sc1
	s_nop 1
	v_pk_mul_f32 v[6:7], v[12:13], s[4:5] op_sel_hi:[1,0]
	v_mov_b64_e32 v[46:47], v[50:51]
	v_mov_b64_e32 v[48:49], v[52:53]
	global_store_dwordx2 v0, v[6:7], s[2:3] offset:72
	v_mov_b64_e32 v[32:33], v[46:47]
	v_accvgpr_read_b32 v6, a252
	v_accvgpr_read_b32 v7, a236
	v_max3_f32 v8, |v32|, |v6|, |v7|
	v_accvgpr_read_b32 v9, a220
	v_accvgpr_read_b32 v14, a204
	v_max3_f32 v8, |v8|, |v9|, |v14|
	v_accvgpr_read_b32 v15, a188
	v_accvgpr_read_b32 v16, a172
	v_max3_f32 v8, |v8|, |v15|, |v16|
	v_accvgpr_read_b32 v10, a156
	v_accvgpr_read_b32 v17, a156
	v_max3_f32 v8, |v8|, |v17|, |v10|
	v_accvgpr_read_b32 v19, a253
	v_accvgpr_read_b32 v20, a237
	v_max3_f32 v10, |v33|, |v19|, |v20|
	v_accvgpr_read_b32 v21, a221
	v_accvgpr_read_b32 v22, a205
	v_max3_f32 v10, |v10|, |v21|, |v22|
	v_accvgpr_read_b32 v23, a189
	v_accvgpr_read_b32 v24, a173
	v_max3_f32 v10, |v10|, |v23|, |v24|
	v_accvgpr_read_b32 v11, a157
	v_mov_b64_e32 v[34:35], v[48:49]
	v_accvgpr_read_b32 v25, a157
	v_max3_f32 v11, |v10|, |v25|, |v11|
	v_accvgpr_read_b32 v27, a254
	v_accvgpr_read_b32 v28, a238
	v_max3_f32 v10, |v34|, |v27|, |v28|
	v_accvgpr_read_b32 v29, a222
	v_accvgpr_read_b32 v30, a206
	v_max3_f32 v10, |v10|, |v29|, |v30|
	v_mov_b32_e32 v3, v32
	v_accvgpr_read_b32 v31, a190
	v_accvgpr_read_b32 v32, a174
	v_max3_f32 v10, |v10|, |v31|, |v32|
	v_accvgpr_read_b32 v12, a158
	v_mov_b32_e32 v18, v33
	v_mov_b32_e32 v26, v34
	v_accvgpr_read_b32 v33, a158
	v_max3_f32 v12, |v10|, |v33|, |v12|
	v_mov_b32_e32 v34, v35
	v_accvgpr_read_b32 v35, a255
	v_accvgpr_read_b32 v36, a239
	v_max3_f32 v10, |v34|, |v35|, |v36|
	v_accvgpr_read_b32 v37, a223
	v_accvgpr_read_b32 v38, a207
	v_max3_f32 v10, |v10|, |v37|, |v38|
	v_accvgpr_read_b32 v13, a159
	v_accvgpr_read_b32 v39, a191
	v_accvgpr_read_b32 v40, a175
	v_max3_f32 v10, |v10|, |v39|, |v40|
	v_accvgpr_read_b32 v41, a159
	v_max3_f32 v13, |v10|, |v41|, |v13|
	s_mov_b64 s[6:7], 0x3000
	s_nop 1
	v_max_f32_dpp v8, v8, v8 quad_perm:[1,0,3,2] row_mask:0xf bank_mask:0xf
	v_max_f32_dpp v11, v11, v11 quad_perm:[1,0,3,2] row_mask:0xf bank_mask:0xf
	v_max_f32_dpp v12, v12, v12 quad_perm:[1,0,3,2] row_mask:0xf bank_mask:0xf
	v_max_f32_dpp v13, v13, v13 quad_perm:[1,0,3,2] row_mask:0xf bank_mask:0xf
	v_max_f32_dpp v8, v8, v8 quad_perm:[2,3,0,1] row_mask:0xf bank_mask:0xf
	v_max_f32_dpp v11, v11, v11 quad_perm:[2,3,0,1] row_mask:0xf bank_mask:0xf
	v_max_f32_dpp v12, v12, v12 quad_perm:[2,3,0,1] row_mask:0xf bank_mask:0xf
	v_max_f32_dpp v13, v13, v13 quad_perm:[2,3,0,1] row_mask:0xf bank_mask:0xf
	v_max_f32_dpp v8, v8, v8 row_half_mirror row_mask:0xf bank_mask:0xf
	v_max_f32_dpp v11, v11, v11 row_half_mirror row_mask:0xf bank_mask:0xf
	v_max_f32_dpp v12, v12, v12 row_half_mirror row_mask:0xf bank_mask:0xf
	v_max_f32_dpp v13, v13, v13 row_half_mirror row_mask:0xf bank_mask:0xf
	v_max_f32_dpp v8, v8, v8 row_mirror row_mask:0xf bank_mask:0xf
	v_max_f32_dpp v11, v11, v11 row_mirror row_mask:0xf bank_mask:0xf
	v_max_f32_dpp v12, v12, v12 row_mirror row_mask:0xf bank_mask:0xf
	v_max_f32_dpp v13, v13, v13 row_mirror row_mask:0xf bank_mask:0xf
	s_nop 0
	ds_swizzle_b32 v232, v8 offset:swizzle(SWAP,16)
	ds_swizzle_b32 v233, v11 offset:swizzle(SWAP,16)
	ds_swizzle_b32 v234, v12 offset:swizzle(SWAP,16)
	ds_swizzle_b32 v235, v13 offset:swizzle(SWAP,16)
	s_waitcnt lgkmcnt(0)
	v_max_f32_e32 v10, v8, v232
	v_rcp_f32_e32 v8, v10
	v_cmp_lt_f32_e32 vcc, 0, v10
	s_waitcnt lgkmcnt(0)
	v_max_f32_e32 v11, v11, v233
	s_waitcnt lgkmcnt(0)
	v_max_f32_e32 v12, v12, v234
	v_cndmask_b32_e32 v42, 0, v8, vcc
	v_mul_f32_e32 v3, v42, v3
	v_mul_f32_e32 v6, v42, v6
	v_cvt_pknorm_i16_f32 v6, v3, v6
	v_mul_f32_e32 v3, v42, v7
	v_mul_f32_e32 v7, v42, v9
	v_cvt_pknorm_i16_f32 v7, v3, v7
	v_pk_mul_f32 v[224:225], v[14:15], v[42:43] op_sel_hi:[1,0]
	v_pk_mul_f32 v[226:227], v[16:17], v[42:43] op_sel_hi:[1,0]
	v_cvt_pknorm_i16_f32 v8, v224, v225
	v_cvt_pknorm_i16_f32 v9, v226, v227
	v_rcp_f32_e32 v3, v11
	v_cmp_lt_f32_e32 vcc, 0, v11
	v_lshl_add_u64 v[14:15], v[4:5], 0, s[6:7]
	global_store_dwordx4 v[14:15], v[6:9], off sc0 sc1
	s_nop 1
	s_mov_b64 s[6:7], 0x3200
	v_cndmask_b32_e32 v3, 0, v3, vcc
	v_pk_mul_f32 v[228:229], v[18:19], v[2:3] op_sel:[0,1] op_sel_hi:[1,1]
	v_pk_mul_f32 v[230:231], v[20:21], v[2:3] op_sel:[0,1] op_sel_hi:[1,1]
	v_cvt_pknorm_i16_f32 v6, v228, v229
	v_cvt_pknorm_i16_f32 v7, v230, v231
	v_pk_mul_f32 v[224:225], v[22:23], v[2:3] op_sel:[0,1] op_sel_hi:[1,1]
	v_pk_mul_f32 v[226:227], v[24:25], v[2:3] op_sel:[0,1] op_sel_hi:[1,1]
	v_cvt_pknorm_i16_f32 v8, v224, v225
	v_cvt_pknorm_i16_f32 v9, v226, v227
	v_rcp_f32_e32 v3, v12
	v_cmp_lt_f32_e32 vcc, 0, v12
	v_lshl_add_u64 v[14:15], v[4:5], 0, s[6:7]
	global_store_dwordx4 v[14:15], v[6:9], off sc0 sc1
	s_nop 1
	v_pk_mul_f32 v[6:7], v[10:11], s[4:5] op_sel_hi:[1,0]
	v_cndmask_b32_e32 v3, 0, v3, vcc
	global_store_dwordx2 v0, v[6:7], s[2:3] offset:96
	v_pk_mul_f32 v[228:229], v[26:27], v[2:3] op_sel:[0,1] op_sel_hi:[1,1]
	v_pk_mul_f32 v[230:231], v[28:29], v[2:3] op_sel:[0,1] op_sel_hi:[1,1]
	v_cvt_pknorm_i16_f32 v6, v228, v229
	v_cvt_pknorm_i16_f32 v7, v230, v231
	v_pk_mul_f32 v[224:225], v[30:31], v[2:3] op_sel:[0,1] op_sel_hi:[1,1]
	v_pk_mul_f32 v[226:227], v[32:33], v[2:3] op_sel:[0,1] op_sel_hi:[1,1]
	v_cvt_pknorm_i16_f32 v8, v224, v225
	s_waitcnt lgkmcnt(0)
	v_max_f32_e32 v13, v13, v235
	v_cvt_pknorm_i16_f32 v9, v226, v227
	v_rcp_f32_e32 v3, v13
	v_cmp_lt_f32_e32 vcc, 0, v13
	s_mov_b64 s[6:7], 0x3400
	v_lshl_add_u64 v[10:11], v[4:5], 0, s[6:7]
	v_cndmask_b32_e32 v3, 0, v3, vcc
	global_store_dwordx4 v[10:11], v[6:9], off sc0 sc1
	s_nop 1
	v_pk_mul_f32 v[228:229], v[34:35], v[2:3] op_sel:[0,1] op_sel_hi:[1,1]
	v_pk_mul_f32 v[230:231], v[36:37], v[2:3] op_sel:[0,1] op_sel_hi:[1,1]
	v_cvt_pknorm_i16_f32 v6, v228, v229
	v_cvt_pknorm_i16_f32 v7, v230, v231
	v_pk_mul_f32 v[224:225], v[38:39], v[2:3] op_sel:[0,1] op_sel_hi:[1,1]
	v_pk_mul_f32 v[226:227], v[40:41], v[2:3] op_sel:[0,1] op_sel_hi:[1,1]
	v_cvt_pknorm_i16_f32 v8, v224, v225
	s_mov_b64 s[6:7], 0x3600
	v_cvt_pknorm_i16_f32 v9, v226, v227
	v_lshl_add_u64 v[10:11], v[4:5], 0, s[6:7]
	global_store_dwordx4 v[10:11], v[6:9], off sc0 sc1
	s_nop 1
	v_pk_mul_f32 v[6:7], v[12:13], s[4:5] op_sel_hi:[1,0]
	global_store_dwordx2 v0, v[6:7], s[2:3] offset:104
	v_accvgpr_read_b32 v3, a0
	v_accvgpr_read_b32 v6, a16
	v_accvgpr_read_b32 v7, a32
	v_max3_f32 v8, |v3|, |v6|, |v7|
	v_accvgpr_read_b32 v9, a48
	v_accvgpr_read_b32 v14, a64
	v_max3_f32 v8, |v8|, |v9|, |v14|
	v_accvgpr_read_b32 v15, a112
	v_accvgpr_read_b32 v16, a128
	v_max3_f32 v8, |v8|, |v15|, |v16|
	v_accvgpr_read_b32 v10, a80
	v_accvgpr_read_b32 v17, a80
	v_max3_f32 v8, |v8|, |v17|, |v10|
	v_accvgpr_read_b32 v18, a1
	v_accvgpr_read_b32 v19, a17
	v_accvgpr_read_b32 v20, a33
	v_max3_f32 v10, |v18|, |v19|, |v20|
	v_accvgpr_read_b32 v21, a49
	v_accvgpr_read_b32 v22, a65
	v_max3_f32 v10, |v10|, |v21|, |v22|
	v_accvgpr_read_b32 v23, a113
	v_accvgpr_read_b32 v24, a129
	v_max3_f32 v10, |v10|, |v23|, |v24|
	v_accvgpr_read_b32 v11, a81
	v_accvgpr_read_b32 v25, a81
	v_max3_f32 v11, |v10|, |v25|, |v11|
	v_accvgpr_read_b32 v26, a2
	v_accvgpr_read_b32 v27, a18
	v_accvgpr_read_b32 v28, a34
	v_max3_f32 v10, |v26|, |v27|, |v28|
	v_accvgpr_read_b32 v29, a50
	v_accvgpr_read_b32 v30, a66
	v_max3_f32 v10, |v10|, |v29|, |v30|
	v_accvgpr_read_b32 v31, a114
	v_accvgpr_read_b32 v32, a130
	v_max3_f32 v10, |v10|, |v31|, |v32|
	v_accvgpr_read_b32 v12, a82
	v_accvgpr_read_b32 v33, a82
	v_max3_f32 v12, |v10|, |v33|, |v12|
	v_accvgpr_read_b32 v34, a3
	v_accvgpr_read_b32 v35, a19
	v_accvgpr_read_b32 v36, a35
	v_max3_f32 v10, |v34|, |v35|, |v36|
	v_accvgpr_read_b32 v37, a51
	v_accvgpr_read_b32 v38, a67
	v_max3_f32 v10, |v10|, |v37|, |v38|
	v_accvgpr_read_b32 v13, a83
	v_accvgpr_read_b32 v39, a115
	v_accvgpr_read_b32 v40, a131
	v_max3_f32 v10, |v10|, |v39|, |v40|
	v_accvgpr_read_b32 v41, a83
	v_max3_f32 v13, |v10|, |v41|, |v13|
	s_mov_b64 s[6:7], 0x4000
	s_nop 1
	v_max_f32_dpp v8, v8, v8 quad_perm:[1,0,3,2] row_mask:0xf bank_mask:0xf
	v_max_f32_dpp v11, v11, v11 quad_perm:[1,0,3,2] row_mask:0xf bank_mask:0xf
	v_max_f32_dpp v12, v12, v12 quad_perm:[1,0,3,2] row_mask:0xf bank_mask:0xf
	v_max_f32_dpp v13, v13, v13 quad_perm:[1,0,3,2] row_mask:0xf bank_mask:0xf
	v_max_f32_dpp v8, v8, v8 quad_perm:[2,3,0,1] row_mask:0xf bank_mask:0xf
	v_max_f32_dpp v11, v11, v11 quad_perm:[2,3,0,1] row_mask:0xf bank_mask:0xf
	v_max_f32_dpp v12, v12, v12 quad_perm:[2,3,0,1] row_mask:0xf bank_mask:0xf
	v_max_f32_dpp v13, v13, v13 quad_perm:[2,3,0,1] row_mask:0xf bank_mask:0xf
	v_max_f32_dpp v8, v8, v8 row_half_mirror row_mask:0xf bank_mask:0xf
	v_max_f32_dpp v11, v11, v11 row_half_mirror row_mask:0xf bank_mask:0xf
	v_max_f32_dpp v12, v12, v12 row_half_mirror row_mask:0xf bank_mask:0xf
	v_max_f32_dpp v13, v13, v13 row_half_mirror row_mask:0xf bank_mask:0xf
	v_max_f32_dpp v8, v8, v8 row_mirror row_mask:0xf bank_mask:0xf
	v_max_f32_dpp v11, v11, v11 row_mirror row_mask:0xf bank_mask:0xf
	v_max_f32_dpp v12, v12, v12 row_mirror row_mask:0xf bank_mask:0xf
	v_max_f32_dpp v13, v13, v13 row_mirror row_mask:0xf bank_mask:0xf
	s_nop 0
	ds_swizzle_b32 v232, v8 offset:swizzle(SWAP,16)
	ds_swizzle_b32 v233, v11 offset:swizzle(SWAP,16)
	ds_swizzle_b32 v234, v12 offset:swizzle(SWAP,16)
	ds_swizzle_b32 v235, v13 offset:swizzle(SWAP,16)
	s_waitcnt lgkmcnt(0)
	v_max_f32_e32 v10, v8, v232
	v_rcp_f32_e32 v8, v10
	v_cmp_lt_f32_e32 vcc, 0, v10
	s_waitcnt lgkmcnt(0)
	v_max_f32_e32 v11, v11, v233
	s_waitcnt lgkmcnt(0)
	v_max_f32_e32 v12, v12, v234
	v_cndmask_b32_e32 v42, 0, v8, vcc
	v_mul_f32_e32 v3, v42, v3
	v_mul_f32_e32 v6, v42, v6
	v_cvt_pknorm_i16_f32 v6, v3, v6
	v_mul_f32_e32 v3, v42, v7
	v_mul_f32_e32 v7, v42, v9
	v_cvt_pknorm_i16_f32 v7, v3, v7
	v_pk_mul_f32 v[228:229], v[14:15], v[42:43] op_sel_hi:[1,0]
	v_pk_mul_f32 v[230:231], v[16:17], v[42:43] op_sel_hi:[1,0]
	v_cvt_pknorm_i16_f32 v8, v228, v229
	v_cvt_pknorm_i16_f32 v9, v230, v231
	v_rcp_f32_e32 v3, v11
	v_cmp_lt_f32_e32 vcc, 0, v11
	v_lshl_add_u64 v[14:15], v[4:5], 0, s[6:7]
	global_store_dwordx4 v[14:15], v[6:9], off sc0 sc1
	s_nop 1
	s_mov_b64 s[6:7], 0x4200
	v_cndmask_b32_e32 v3, 0, v3, vcc
	v_pk_mul_f32 v[224:225], v[18:19], v[2:3] op_sel:[0,1] op_sel_hi:[1,1]
	v_pk_mul_f32 v[226:227], v[20:21], v[2:3] op_sel:[0,1] op_sel_hi:[1,1]
	v_cvt_pknorm_i16_f32 v6, v224, v225
	v_cvt_pknorm_i16_f32 v7, v226, v227
	v_pk_mul_f32 v[228:229], v[22:23], v[2:3] op_sel:[0,1] op_sel_hi:[1,1]
	v_pk_mul_f32 v[230:231], v[24:25], v[2:3] op_sel:[0,1] op_sel_hi:[1,1]
	v_cvt_pknorm_i16_f32 v8, v228, v229
	v_cvt_pknorm_i16_f32 v9, v230, v231
	v_rcp_f32_e32 v3, v12
	v_cmp_lt_f32_e32 vcc, 0, v12
	v_lshl_add_u64 v[14:15], v[4:5], 0, s[6:7]
	global_store_dwordx4 v[14:15], v[6:9], off sc0 sc1
	s_nop 1
	v_pk_mul_f32 v[6:7], v[10:11], s[4:5] op_sel_hi:[1,0]
	v_cndmask_b32_e32 v3, 0, v3, vcc
	global_store_dwordx2 v0, v[6:7], s[2:3] offset:128
	v_pk_mul_f32 v[224:225], v[26:27], v[2:3] op_sel:[0,1] op_sel_hi:[1,1]
	v_pk_mul_f32 v[226:227], v[28:29], v[2:3] op_sel:[0,1] op_sel_hi:[1,1]
	v_cvt_pknorm_i16_f32 v6, v224, v225
	v_cvt_pknorm_i16_f32 v7, v226, v227
	v_pk_mul_f32 v[228:229], v[30:31], v[2:3] op_sel:[0,1] op_sel_hi:[1,1]
	v_pk_mul_f32 v[230:231], v[32:33], v[2:3] op_sel:[0,1] op_sel_hi:[1,1]
	v_cvt_pknorm_i16_f32 v8, v228, v229
	s_waitcnt lgkmcnt(0)
	v_max_f32_e32 v13, v13, v235
	v_cvt_pknorm_i16_f32 v9, v230, v231
	v_rcp_f32_e32 v3, v13
	v_cmp_lt_f32_e32 vcc, 0, v13
	s_mov_b64 s[6:7], 0x4400
	v_lshl_add_u64 v[10:11], v[4:5], 0, s[6:7]
	v_cndmask_b32_e32 v3, 0, v3, vcc
	global_store_dwordx4 v[10:11], v[6:9], off sc0 sc1
	s_nop 1
	v_pk_mul_f32 v[224:225], v[34:35], v[2:3] op_sel:[0,1] op_sel_hi:[1,1]
	v_pk_mul_f32 v[226:227], v[36:37], v[2:3] op_sel:[0,1] op_sel_hi:[1,1]
	v_cvt_pknorm_i16_f32 v6, v224, v225
	v_cvt_pknorm_i16_f32 v7, v226, v227
	v_pk_mul_f32 v[228:229], v[38:39], v[2:3] op_sel:[0,1] op_sel_hi:[1,1]
	v_pk_mul_f32 v[230:231], v[40:41], v[2:3] op_sel:[0,1] op_sel_hi:[1,1]
	v_cvt_pknorm_i16_f32 v8, v228, v229
	s_mov_b64 s[6:7], 0x4600
	v_cvt_pknorm_i16_f32 v9, v230, v231
	v_lshl_add_u64 v[10:11], v[4:5], 0, s[6:7]
	global_store_dwordx4 v[10:11], v[6:9], off sc0 sc1
	s_nop 1
	v_pk_mul_f32 v[6:7], v[12:13], s[4:5] op_sel_hi:[1,0]
	global_store_dwordx2 v0, v[6:7], s[2:3] offset:136
	v_accvgpr_read_b32 v3, a4
	v_accvgpr_read_b32 v6, a20
	v_accvgpr_read_b32 v7, a36
	v_max3_f32 v8, |v3|, |v6|, |v7|
	v_accvgpr_read_b32 v9, a52
	v_accvgpr_read_b32 v14, a68
	v_max3_f32 v8, |v8|, |v9|, |v14|
	v_accvgpr_read_b32 v15, a116
	v_accvgpr_read_b32 v16, a132
	v_max3_f32 v8, |v8|, |v15|, |v16|
	v_accvgpr_read_b32 v10, a84
	v_accvgpr_read_b32 v17, a84
	v_max3_f32 v8, |v8|, |v17|, |v10|
	v_accvgpr_read_b32 v18, a5
	v_accvgpr_read_b32 v19, a21
	v_accvgpr_read_b32 v20, a37
	v_max3_f32 v10, |v18|, |v19|, |v20|
	v_accvgpr_read_b32 v21, a53
	v_accvgpr_read_b32 v22, a69
	v_max3_f32 v10, |v10|, |v21|, |v22|
	v_accvgpr_read_b32 v23, a117
	v_accvgpr_read_b32 v24, a133
	v_max3_f32 v10, |v10|, |v23|, |v24|
	v_accvgpr_read_b32 v11, a85
	v_accvgpr_read_b32 v25, a85
	v_max3_f32 v11, |v10|, |v25|, |v11|
	v_accvgpr_read_b32 v26, a6
	v_accvgpr_read_b32 v27, a22
	v_accvgpr_read_b32 v28, a38
	v_max3_f32 v10, |v26|, |v27|, |v28|
	v_accvgpr_read_b32 v29, a54
	v_accvgpr_read_b32 v30, a70
	v_max3_f32 v10, |v10|, |v29|, |v30|
	v_accvgpr_read_b32 v31, a118
	v_accvgpr_read_b32 v32, a134
	v_max3_f32 v10, |v10|, |v31|, |v32|
	v_accvgpr_read_b32 v12, a86
	v_accvgpr_read_b32 v33, a86
	v_max3_f32 v12, |v10|, |v33|, |v12|
	v_accvgpr_read_b32 v34, a7
	v_accvgpr_read_b32 v35, a23
	v_accvgpr_read_b32 v36, a39
	v_max3_f32 v10, |v34|, |v35|, |v36|
	v_accvgpr_read_b32 v37, a55
	v_accvgpr_read_b32 v38, a71
	v_max3_f32 v10, |v10|, |v37|, |v38|
	v_accvgpr_read_b32 v13, a87
	v_accvgpr_read_b32 v39, a119
	v_accvgpr_read_b32 v40, a135
	v_max3_f32 v10, |v10|, |v39|, |v40|
	v_accvgpr_read_b32 v41, a87
	v_max3_f32 v13, |v10|, |v41|, |v13|
	s_mov_b64 s[6:7], 0x5000
	s_nop 1
	v_max_f32_dpp v8, v8, v8 quad_perm:[1,0,3,2] row_mask:0xf bank_mask:0xf
	v_max_f32_dpp v11, v11, v11 quad_perm:[1,0,3,2] row_mask:0xf bank_mask:0xf
	v_max_f32_dpp v12, v12, v12 quad_perm:[1,0,3,2] row_mask:0xf bank_mask:0xf
	v_max_f32_dpp v13, v13, v13 quad_perm:[1,0,3,2] row_mask:0xf bank_mask:0xf
	v_max_f32_dpp v8, v8, v8 quad_perm:[2,3,0,1] row_mask:0xf bank_mask:0xf
	v_max_f32_dpp v11, v11, v11 quad_perm:[2,3,0,1] row_mask:0xf bank_mask:0xf
	v_max_f32_dpp v12, v12, v12 quad_perm:[2,3,0,1] row_mask:0xf bank_mask:0xf
	v_max_f32_dpp v13, v13, v13 quad_perm:[2,3,0,1] row_mask:0xf bank_mask:0xf
	v_max_f32_dpp v8, v8, v8 row_half_mirror row_mask:0xf bank_mask:0xf
	v_max_f32_dpp v11, v11, v11 row_half_mirror row_mask:0xf bank_mask:0xf
	v_max_f32_dpp v12, v12, v12 row_half_mirror row_mask:0xf bank_mask:0xf
	v_max_f32_dpp v13, v13, v13 row_half_mirror row_mask:0xf bank_mask:0xf
	v_max_f32_dpp v8, v8, v8 row_mirror row_mask:0xf bank_mask:0xf
	v_max_f32_dpp v11, v11, v11 row_mirror row_mask:0xf bank_mask:0xf
	v_max_f32_dpp v12, v12, v12 row_mirror row_mask:0xf bank_mask:0xf
	v_max_f32_dpp v13, v13, v13 row_mirror row_mask:0xf bank_mask:0xf
	s_nop 0
	ds_swizzle_b32 v232, v8 offset:swizzle(SWAP,16)
	ds_swizzle_b32 v233, v11 offset:swizzle(SWAP,16)
	ds_swizzle_b32 v234, v12 offset:swizzle(SWAP,16)
	ds_swizzle_b32 v235, v13 offset:swizzle(SWAP,16)
	s_waitcnt lgkmcnt(0)
	v_max_f32_e32 v10, v8, v232
	v_rcp_f32_e32 v8, v10
	v_cmp_lt_f32_e32 vcc, 0, v10
	s_waitcnt lgkmcnt(0)
	v_max_f32_e32 v11, v11, v233
	s_waitcnt lgkmcnt(0)
	v_max_f32_e32 v12, v12, v234
	v_cndmask_b32_e32 v42, 0, v8, vcc
	v_mul_f32_e32 v3, v42, v3
	v_mul_f32_e32 v6, v42, v6
	v_cvt_pknorm_i16_f32 v6, v3, v6
	v_mul_f32_e32 v3, v42, v7
	v_mul_f32_e32 v7, v42, v9
	v_cvt_pknorm_i16_f32 v7, v3, v7
	v_pk_mul_f32 v[224:225], v[14:15], v[42:43] op_sel_hi:[1,0]
	v_pk_mul_f32 v[226:227], v[16:17], v[42:43] op_sel_hi:[1,0]
	v_cvt_pknorm_i16_f32 v8, v224, v225
	v_cvt_pknorm_i16_f32 v9, v226, v227
	v_rcp_f32_e32 v3, v11
	v_cmp_lt_f32_e32 vcc, 0, v11
	v_lshl_add_u64 v[14:15], v[4:5], 0, s[6:7]
	global_store_dwordx4 v[14:15], v[6:9], off sc0 sc1
	s_nop 1
	s_mov_b64 s[6:7], 0x5200
	v_cndmask_b32_e32 v3, 0, v3, vcc
	v_pk_mul_f32 v[228:229], v[18:19], v[2:3] op_sel:[0,1] op_sel_hi:[1,1]
	v_pk_mul_f32 v[230:231], v[20:21], v[2:3] op_sel:[0,1] op_sel_hi:[1,1]
	v_cvt_pknorm_i16_f32 v6, v228, v229
	v_cvt_pknorm_i16_f32 v7, v230, v231
	v_pk_mul_f32 v[224:225], v[22:23], v[2:3] op_sel:[0,1] op_sel_hi:[1,1]
	v_pk_mul_f32 v[226:227], v[24:25], v[2:3] op_sel:[0,1] op_sel_hi:[1,1]
	v_cvt_pknorm_i16_f32 v8, v224, v225
	v_cvt_pknorm_i16_f32 v9, v226, v227
	v_rcp_f32_e32 v3, v12
	v_cmp_lt_f32_e32 vcc, 0, v12
	v_lshl_add_u64 v[14:15], v[4:5], 0, s[6:7]
	global_store_dwordx4 v[14:15], v[6:9], off sc0 sc1
	s_nop 1
	v_pk_mul_f32 v[6:7], v[10:11], s[4:5] op_sel_hi:[1,0]
	v_cndmask_b32_e32 v3, 0, v3, vcc
	global_store_dwordx2 v0, v[6:7], s[2:3] offset:160
	v_pk_mul_f32 v[228:229], v[26:27], v[2:3] op_sel:[0,1] op_sel_hi:[1,1]
	v_pk_mul_f32 v[230:231], v[28:29], v[2:3] op_sel:[0,1] op_sel_hi:[1,1]
	v_cvt_pknorm_i16_f32 v6, v228, v229
	v_cvt_pknorm_i16_f32 v7, v230, v231
	v_pk_mul_f32 v[224:225], v[30:31], v[2:3] op_sel:[0,1] op_sel_hi:[1,1]
	v_pk_mul_f32 v[226:227], v[32:33], v[2:3] op_sel:[0,1] op_sel_hi:[1,1]
	v_cvt_pknorm_i16_f32 v8, v224, v225
	s_waitcnt lgkmcnt(0)
	v_max_f32_e32 v13, v13, v235
	v_cvt_pknorm_i16_f32 v9, v226, v227
	v_rcp_f32_e32 v3, v13
	v_cmp_lt_f32_e32 vcc, 0, v13
	s_mov_b64 s[6:7], 0x5400
	v_lshl_add_u64 v[10:11], v[4:5], 0, s[6:7]
	v_cndmask_b32_e32 v3, 0, v3, vcc
	global_store_dwordx4 v[10:11], v[6:9], off sc0 sc1
	s_nop 1
	v_pk_mul_f32 v[228:229], v[34:35], v[2:3] op_sel:[0,1] op_sel_hi:[1,1]
	v_pk_mul_f32 v[230:231], v[36:37], v[2:3] op_sel:[0,1] op_sel_hi:[1,1]
	v_cvt_pknorm_i16_f32 v6, v228, v229
	v_cvt_pknorm_i16_f32 v7, v230, v231
	v_pk_mul_f32 v[224:225], v[38:39], v[2:3] op_sel:[0,1] op_sel_hi:[1,1]
	v_pk_mul_f32 v[226:227], v[40:41], v[2:3] op_sel:[0,1] op_sel_hi:[1,1]
	v_cvt_pknorm_i16_f32 v8, v224, v225
	s_mov_b64 s[6:7], 0x5600
	v_cvt_pknorm_i16_f32 v9, v226, v227
	v_lshl_add_u64 v[10:11], v[4:5], 0, s[6:7]
	global_store_dwordx4 v[10:11], v[6:9], off sc0 sc1
	s_nop 1
	v_pk_mul_f32 v[6:7], v[12:13], s[4:5] op_sel_hi:[1,0]
	global_store_dwordx2 v0, v[6:7], s[2:3] offset:168
	v_accvgpr_read_b32 v3, a8
	v_accvgpr_read_b32 v6, a24
	v_accvgpr_read_b32 v7, a40
	v_max3_f32 v8, |v3|, |v6|, |v7|
	v_accvgpr_read_b32 v9, a56
	v_accvgpr_read_b32 v14, a72
	v_max3_f32 v8, |v8|, |v9|, |v14|
	v_accvgpr_read_b32 v15, a120
	v_accvgpr_read_b32 v16, a136
	v_max3_f32 v8, |v8|, |v15|, |v16|
	v_accvgpr_read_b32 v10, a88
	v_accvgpr_read_b32 v17, a88
	v_max3_f32 v8, |v8|, |v17|, |v10|
	v_accvgpr_read_b32 v18, a9
	v_accvgpr_read_b32 v19, a25
	v_accvgpr_read_b32 v20, a41
	v_max3_f32 v10, |v18|, |v19|, |v20|
	v_accvgpr_read_b32 v21, a57
	v_accvgpr_read_b32 v22, a73
	v_max3_f32 v10, |v10|, |v21|, |v22|
	v_accvgpr_read_b32 v23, a121
	v_accvgpr_read_b32 v24, a137
	v_max3_f32 v10, |v10|, |v23|, |v24|
	v_accvgpr_read_b32 v11, a89
	v_accvgpr_read_b32 v25, a89
	v_max3_f32 v11, |v10|, |v25|, |v11|
	v_accvgpr_read_b32 v26, a10
	v_accvgpr_read_b32 v27, a26
	v_accvgpr_read_b32 v28, a42
	v_max3_f32 v10, |v26|, |v27|, |v28|
	v_accvgpr_read_b32 v29, a58
	v_accvgpr_read_b32 v30, a74
	v_max3_f32 v10, |v10|, |v29|, |v30|
	v_accvgpr_read_b32 v31, a122
	v_accvgpr_read_b32 v32, a138
	v_max3_f32 v10, |v10|, |v31|, |v32|
	v_accvgpr_read_b32 v12, a90
	v_accvgpr_read_b32 v33, a90
	v_max3_f32 v12, |v10|, |v33|, |v12|
	v_accvgpr_read_b32 v34, a11
	v_accvgpr_read_b32 v35, a27
	v_accvgpr_read_b32 v36, a43
	v_max3_f32 v10, |v34|, |v35|, |v36|
	v_accvgpr_read_b32 v37, a59
	v_accvgpr_read_b32 v38, a75
	v_max3_f32 v10, |v10|, |v37|, |v38|
	v_accvgpr_read_b32 v13, a91
	v_accvgpr_read_b32 v39, a123
	v_accvgpr_read_b32 v40, a139
	v_max3_f32 v10, |v10|, |v39|, |v40|
	v_accvgpr_read_b32 v41, a91
	v_max3_f32 v13, |v10|, |v41|, |v13|
	s_mov_b64 s[6:7], 0x6000
	s_nop 1
	v_max_f32_dpp v8, v8, v8 quad_perm:[1,0,3,2] row_mask:0xf bank_mask:0xf
	v_max_f32_dpp v11, v11, v11 quad_perm:[1,0,3,2] row_mask:0xf bank_mask:0xf
	v_max_f32_dpp v12, v12, v12 quad_perm:[1,0,3,2] row_mask:0xf bank_mask:0xf
	v_max_f32_dpp v13, v13, v13 quad_perm:[1,0,3,2] row_mask:0xf bank_mask:0xf
	v_max_f32_dpp v8, v8, v8 quad_perm:[2,3,0,1] row_mask:0xf bank_mask:0xf
	v_max_f32_dpp v11, v11, v11 quad_perm:[2,3,0,1] row_mask:0xf bank_mask:0xf
	v_max_f32_dpp v12, v12, v12 quad_perm:[2,3,0,1] row_mask:0xf bank_mask:0xf
	v_max_f32_dpp v13, v13, v13 quad_perm:[2,3,0,1] row_mask:0xf bank_mask:0xf
	v_max_f32_dpp v8, v8, v8 row_half_mirror row_mask:0xf bank_mask:0xf
	v_max_f32_dpp v11, v11, v11 row_half_mirror row_mask:0xf bank_mask:0xf
	v_max_f32_dpp v12, v12, v12 row_half_mirror row_mask:0xf bank_mask:0xf
	v_max_f32_dpp v13, v13, v13 row_half_mirror row_mask:0xf bank_mask:0xf
	v_max_f32_dpp v8, v8, v8 row_mirror row_mask:0xf bank_mask:0xf
	v_max_f32_dpp v11, v11, v11 row_mirror row_mask:0xf bank_mask:0xf
	v_max_f32_dpp v12, v12, v12 row_mirror row_mask:0xf bank_mask:0xf
	v_max_f32_dpp v13, v13, v13 row_mirror row_mask:0xf bank_mask:0xf
	s_nop 0
	ds_swizzle_b32 v232, v8 offset:swizzle(SWAP,16)
	ds_swizzle_b32 v233, v11 offset:swizzle(SWAP,16)
	ds_swizzle_b32 v234, v12 offset:swizzle(SWAP,16)
	ds_swizzle_b32 v235, v13 offset:swizzle(SWAP,16)
	s_waitcnt lgkmcnt(0)
	v_max_f32_e32 v10, v8, v232
	v_rcp_f32_e32 v8, v10
	v_cmp_lt_f32_e32 vcc, 0, v10
	s_waitcnt lgkmcnt(0)
	v_max_f32_e32 v11, v11, v233
	s_waitcnt lgkmcnt(0)
	v_max_f32_e32 v12, v12, v234
	v_cndmask_b32_e32 v42, 0, v8, vcc
	v_mul_f32_e32 v3, v42, v3
	v_mul_f32_e32 v6, v42, v6
	v_cvt_pknorm_i16_f32 v6, v3, v6
	v_mul_f32_e32 v3, v42, v7
	v_mul_f32_e32 v7, v42, v9
	v_cvt_pknorm_i16_f32 v7, v3, v7
	v_pk_mul_f32 v[228:229], v[14:15], v[42:43] op_sel_hi:[1,0]
	v_pk_mul_f32 v[230:231], v[16:17], v[42:43] op_sel_hi:[1,0]
	v_cvt_pknorm_i16_f32 v8, v228, v229
	v_cvt_pknorm_i16_f32 v9, v230, v231
	v_rcp_f32_e32 v3, v11
	v_cmp_lt_f32_e32 vcc, 0, v11
	v_lshl_add_u64 v[14:15], v[4:5], 0, s[6:7]
	global_store_dwordx4 v[14:15], v[6:9], off sc0 sc1
	s_nop 1
	s_mov_b64 s[6:7], 0x6200
	v_cndmask_b32_e32 v3, 0, v3, vcc
	v_pk_mul_f32 v[224:225], v[18:19], v[2:3] op_sel:[0,1] op_sel_hi:[1,1]
	v_pk_mul_f32 v[226:227], v[20:21], v[2:3] op_sel:[0,1] op_sel_hi:[1,1]
	v_cvt_pknorm_i16_f32 v6, v224, v225
	v_cvt_pknorm_i16_f32 v7, v226, v227
	v_pk_mul_f32 v[228:229], v[22:23], v[2:3] op_sel:[0,1] op_sel_hi:[1,1]
	v_pk_mul_f32 v[230:231], v[24:25], v[2:3] op_sel:[0,1] op_sel_hi:[1,1]
	v_cvt_pknorm_i16_f32 v8, v228, v229
	v_cvt_pknorm_i16_f32 v9, v230, v231
	v_rcp_f32_e32 v3, v12
	v_cmp_lt_f32_e32 vcc, 0, v12
	v_lshl_add_u64 v[14:15], v[4:5], 0, s[6:7]
	global_store_dwordx4 v[14:15], v[6:9], off sc0 sc1
	s_nop 1
	v_pk_mul_f32 v[6:7], v[10:11], s[4:5] op_sel_hi:[1,0]
	v_cndmask_b32_e32 v3, 0, v3, vcc
	global_store_dwordx2 v0, v[6:7], s[2:3] offset:192
	v_pk_mul_f32 v[224:225], v[26:27], v[2:3] op_sel:[0,1] op_sel_hi:[1,1]
	v_pk_mul_f32 v[226:227], v[28:29], v[2:3] op_sel:[0,1] op_sel_hi:[1,1]
	v_cvt_pknorm_i16_f32 v6, v224, v225
	v_cvt_pknorm_i16_f32 v7, v226, v227
	v_pk_mul_f32 v[228:229], v[30:31], v[2:3] op_sel:[0,1] op_sel_hi:[1,1]
	v_pk_mul_f32 v[230:231], v[32:33], v[2:3] op_sel:[0,1] op_sel_hi:[1,1]
	v_cvt_pknorm_i16_f32 v8, v228, v229
	s_waitcnt lgkmcnt(0)
	v_max_f32_e32 v13, v13, v235
	v_cvt_pknorm_i16_f32 v9, v230, v231
	v_rcp_f32_e32 v3, v13
	v_cmp_lt_f32_e32 vcc, 0, v13
	s_mov_b64 s[6:7], 0x6400
	v_lshl_add_u64 v[10:11], v[4:5], 0, s[6:7]
	v_cndmask_b32_e32 v3, 0, v3, vcc
	global_store_dwordx4 v[10:11], v[6:9], off sc0 sc1
	s_nop 1
	v_pk_mul_f32 v[224:225], v[34:35], v[2:3] op_sel:[0,1] op_sel_hi:[1,1]
	v_pk_mul_f32 v[226:227], v[36:37], v[2:3] op_sel:[0,1] op_sel_hi:[1,1]
	v_cvt_pknorm_i16_f32 v6, v224, v225
	v_cvt_pknorm_i16_f32 v7, v226, v227
	v_pk_mul_f32 v[228:229], v[38:39], v[2:3] op_sel:[0,1] op_sel_hi:[1,1]
	v_pk_mul_f32 v[230:231], v[40:41], v[2:3] op_sel:[0,1] op_sel_hi:[1,1]
	v_cvt_pknorm_i16_f32 v8, v228, v229
	s_mov_b64 s[6:7], 0x6600
	v_cvt_pknorm_i16_f32 v9, v230, v231
	v_lshl_add_u64 v[10:11], v[4:5], 0, s[6:7]
	global_store_dwordx4 v[10:11], v[6:9], off sc0 sc1
	s_nop 1
	v_pk_mul_f32 v[6:7], v[12:13], s[4:5] op_sel_hi:[1,0]
	global_store_dwordx2 v0, v[6:7], s[2:3] offset:200
	v_accvgpr_read_b32 v3, a12
	v_accvgpr_read_b32 v6, a28
	v_accvgpr_read_b32 v7, a44
	v_max3_f32 v8, |v3|, |v6|, |v7|
	v_accvgpr_read_b32 v9, a60
	v_accvgpr_read_b32 v14, a76
	v_max3_f32 v8, |v8|, |v9|, |v14|
	v_accvgpr_read_b32 v15, a124
	v_accvgpr_read_b32 v16, a140
	v_max3_f32 v8, |v8|, |v15|, |v16|
	v_accvgpr_read_b32 v10, a92
	v_accvgpr_read_b32 v17, a92
	v_max3_f32 v8, |v8|, |v17|, |v10|
	v_accvgpr_read_b32 v18, a13
	v_accvgpr_read_b32 v19, a29
	v_accvgpr_read_b32 v20, a45
	v_max3_f32 v10, |v18|, |v19|, |v20|
	v_accvgpr_read_b32 v21, a61
	v_accvgpr_read_b32 v22, a77
	v_max3_f32 v10, |v10|, |v21|, |v22|
	v_accvgpr_read_b32 v23, a125
	v_accvgpr_read_b32 v24, a141
	v_max3_f32 v10, |v10|, |v23|, |v24|
	v_accvgpr_read_b32 v11, a93
	v_accvgpr_read_b32 v25, a93
	v_max3_f32 v11, |v10|, |v25|, |v11|
	v_accvgpr_read_b32 v26, a14
	v_accvgpr_read_b32 v27, a30
	v_accvgpr_read_b32 v28, a46
	v_max3_f32 v10, |v26|, |v27|, |v28|
	v_accvgpr_read_b32 v29, a62
	v_accvgpr_read_b32 v30, a78
	v_max3_f32 v10, |v10|, |v29|, |v30|
	v_accvgpr_read_b32 v31, a126
	v_accvgpr_read_b32 v32, a142
	v_max3_f32 v10, |v10|, |v31|, |v32|
	v_accvgpr_read_b32 v12, a94
	v_accvgpr_read_b32 v33, a94
	v_max3_f32 v12, |v10|, |v33|, |v12|
	v_accvgpr_read_b32 v34, a15
	v_accvgpr_read_b32 v35, a31
	v_accvgpr_read_b32 v36, a47
	v_max3_f32 v10, |v34|, |v35|, |v36|
	v_accvgpr_read_b32 v37, a63
	v_accvgpr_read_b32 v38, a79
	v_max3_f32 v10, |v10|, |v37|, |v38|
	v_accvgpr_read_b32 v13, a95
	v_accvgpr_read_b32 v39, a127
	v_accvgpr_read_b32 v40, a143
	v_max3_f32 v10, |v10|, |v39|, |v40|
	v_accvgpr_read_b32 v41, a95
	v_max3_f32 v13, |v10|, |v41|, |v13|
	s_mov_b64 s[6:7], 0x7000
	s_nop 1
	v_max_f32_dpp v8, v8, v8 quad_perm:[1,0,3,2] row_mask:0xf bank_mask:0xf
	v_max_f32_dpp v11, v11, v11 quad_perm:[1,0,3,2] row_mask:0xf bank_mask:0xf
	v_max_f32_dpp v12, v12, v12 quad_perm:[1,0,3,2] row_mask:0xf bank_mask:0xf
	v_max_f32_dpp v13, v13, v13 quad_perm:[1,0,3,2] row_mask:0xf bank_mask:0xf
	v_max_f32_dpp v8, v8, v8 quad_perm:[2,3,0,1] row_mask:0xf bank_mask:0xf
	v_max_f32_dpp v11, v11, v11 quad_perm:[2,3,0,1] row_mask:0xf bank_mask:0xf
	v_max_f32_dpp v12, v12, v12 quad_perm:[2,3,0,1] row_mask:0xf bank_mask:0xf
	v_max_f32_dpp v13, v13, v13 quad_perm:[2,3,0,1] row_mask:0xf bank_mask:0xf
	v_max_f32_dpp v8, v8, v8 row_half_mirror row_mask:0xf bank_mask:0xf
	v_max_f32_dpp v11, v11, v11 row_half_mirror row_mask:0xf bank_mask:0xf
	v_max_f32_dpp v12, v12, v12 row_half_mirror row_mask:0xf bank_mask:0xf
	v_max_f32_dpp v13, v13, v13 row_half_mirror row_mask:0xf bank_mask:0xf
	v_max_f32_dpp v8, v8, v8 row_mirror row_mask:0xf bank_mask:0xf
	v_max_f32_dpp v11, v11, v11 row_mirror row_mask:0xf bank_mask:0xf
	v_max_f32_dpp v12, v12, v12 row_mirror row_mask:0xf bank_mask:0xf
	v_max_f32_dpp v13, v13, v13 row_mirror row_mask:0xf bank_mask:0xf
	s_nop 0
	ds_swizzle_b32 v232, v8 offset:swizzle(SWAP,16)
	ds_swizzle_b32 v233, v11 offset:swizzle(SWAP,16)
	ds_swizzle_b32 v234, v12 offset:swizzle(SWAP,16)
	ds_swizzle_b32 v235, v13 offset:swizzle(SWAP,16)
	s_waitcnt lgkmcnt(0)
	v_max_f32_e32 v10, v8, v232
	v_rcp_f32_e32 v8, v10
	v_cmp_lt_f32_e32 vcc, 0, v10
	s_waitcnt lgkmcnt(0)
	v_max_f32_e32 v11, v11, v233
	s_waitcnt lgkmcnt(0)
	v_max_f32_e32 v12, v12, v234
	v_cndmask_b32_e32 v42, 0, v8, vcc
	v_mul_f32_e32 v3, v42, v3
	v_mul_f32_e32 v6, v42, v6
	v_cvt_pknorm_i16_f32 v6, v3, v6
	v_mul_f32_e32 v3, v42, v7
	v_mul_f32_e32 v7, v42, v9
	v_cvt_pknorm_i16_f32 v7, v3, v7
	v_pk_mul_f32 v[224:225], v[14:15], v[42:43] op_sel_hi:[1,0]
	v_pk_mul_f32 v[226:227], v[16:17], v[42:43] op_sel_hi:[1,0]
	v_cvt_pknorm_i16_f32 v8, v224, v225
	v_cvt_pknorm_i16_f32 v9, v226, v227
	v_rcp_f32_e32 v3, v11
	v_cmp_lt_f32_e32 vcc, 0, v11
	v_lshl_add_u64 v[14:15], v[4:5], 0, s[6:7]
	global_store_dwordx4 v[14:15], v[6:9], off sc0 sc1
	s_nop 1
	s_mov_b64 s[6:7], 0x7200
	v_cndmask_b32_e32 v3, 0, v3, vcc
	v_pk_mul_f32 v[228:229], v[18:19], v[2:3] op_sel:[0,1] op_sel_hi:[1,1]
	v_pk_mul_f32 v[230:231], v[20:21], v[2:3] op_sel:[0,1] op_sel_hi:[1,1]
	v_cvt_pknorm_i16_f32 v6, v228, v229
	v_cvt_pknorm_i16_f32 v7, v230, v231
	v_pk_mul_f32 v[224:225], v[22:23], v[2:3] op_sel:[0,1] op_sel_hi:[1,1]
	v_pk_mul_f32 v[226:227], v[24:25], v[2:3] op_sel:[0,1] op_sel_hi:[1,1]
	v_cvt_pknorm_i16_f32 v8, v224, v225
	v_cvt_pknorm_i16_f32 v9, v226, v227
	v_rcp_f32_e32 v3, v12
	v_cmp_lt_f32_e32 vcc, 0, v12
	v_lshl_add_u64 v[14:15], v[4:5], 0, s[6:7]
	global_store_dwordx4 v[14:15], v[6:9], off sc0 sc1
	s_nop 1
	v_pk_mul_f32 v[6:7], v[10:11], s[4:5] op_sel_hi:[1,0]
	v_cndmask_b32_e32 v3, 0, v3, vcc
	global_store_dwordx2 v0, v[6:7], s[2:3] offset:224
	v_pk_mul_f32 v[228:229], v[26:27], v[2:3] op_sel:[0,1] op_sel_hi:[1,1]
	v_pk_mul_f32 v[230:231], v[28:29], v[2:3] op_sel:[0,1] op_sel_hi:[1,1]
	v_cvt_pknorm_i16_f32 v6, v228, v229
	v_cvt_pknorm_i16_f32 v7, v230, v231
	v_pk_mul_f32 v[224:225], v[30:31], v[2:3] op_sel:[0,1] op_sel_hi:[1,1]
	v_pk_mul_f32 v[226:227], v[32:33], v[2:3] op_sel:[0,1] op_sel_hi:[1,1]
	v_cvt_pknorm_i16_f32 v8, v224, v225
	s_waitcnt lgkmcnt(0)
	v_max_f32_e32 v13, v13, v235
	v_cvt_pknorm_i16_f32 v9, v226, v227
	v_rcp_f32_e32 v3, v13
	v_cmp_lt_f32_e32 vcc, 0, v13
	s_mov_b64 s[6:7], 0x7400
	v_lshl_add_u64 v[10:11], v[4:5], 0, s[6:7]
	v_cndmask_b32_e32 v3, 0, v3, vcc
	global_store_dwordx4 v[10:11], v[6:9], off sc0 sc1
	s_nop 1
	v_pk_mul_f32 v[228:229], v[34:35], v[2:3] op_sel:[0,1] op_sel_hi:[1,1]
	v_pk_mul_f32 v[230:231], v[36:37], v[2:3] op_sel:[0,1] op_sel_hi:[1,1]
	v_cvt_pknorm_i16_f32 v6, v228, v229
	v_cvt_pknorm_i16_f32 v7, v230, v231
	v_pk_mul_f32 v[224:225], v[38:39], v[2:3] op_sel:[0,1] op_sel_hi:[1,1]
	v_pk_mul_f32 v[226:227], v[40:41], v[2:3] op_sel:[0,1] op_sel_hi:[1,1]
	v_cvt_pknorm_i16_f32 v8, v224, v225
	s_mov_b64 s[6:7], 0x7600
	v_cvt_pknorm_i16_f32 v9, v226, v227
	v_lshl_add_u64 v[4:5], v[4:5], 0, s[6:7]
	global_store_dwordx4 v[4:5], v[6:9], off sc0 sc1
	s_nop 1
	v_pk_mul_f32 v[4:5], v[12:13], s[4:5] op_sel_hi:[1,0]
	global_store_dwordx2 v0, v[4:5], s[2:3] offset:232
	ds_bpermute_b32 v4, v133, v134
	s_lshl_b64 s[0:1], s[0:1], 2
	s_add_u32 s0, s26, s0
	s_addc_u32 s1, s27, s1
	v_mov_b32_e32 v3, v1
	v_cmp_gt_i32_e32 vcc, 32, v132
	v_lshl_add_u64 v[0:1], s[0:1], 0, v[2:3]
	s_and_saveexec_b64 s[0:1], vcc
	s_cbranch_execz .LBB1_6
	s_waitcnt lgkmcnt(0)
	v_add_f32_e32 v2, v134, v4
	global_store_dword v[0:1], v2, off

	.amdhsa_kernel _Z6k_mainPKDF16_PKfS2_S2_PKmPjPfS6_
		.amdhsa_group_segment_fixed_size 114688
		.amdhsa_private_segment_fixed_size 0
		.amdhsa_kernarg_size 64
		.amdhsa_user_sgpr_count 2
		.amdhsa_user_sgpr_dispatch_ptr 0
		.amdhsa_user_sgpr_queue_ptr 0
		.amdhsa_user_sgpr_kernarg_segment_ptr 1
		.amdhsa_user_sgpr_dispatch_id 0
		.amdhsa_user_sgpr_kernarg_preload_length 0
		.amdhsa_user_sgpr_kernarg_preload_offset 0
		.amdhsa_user_sgpr_private_segment_size 0
		.amdhsa_uses_dynamic_stack 0
		.amdhsa_enable_private_segment 0
		.amdhsa_system_sgpr_workgroup_id_x 1
		.amdhsa_system_sgpr_workgroup_id_y 0
		.amdhsa_system_sgpr_workgroup_id_z 0
		.amdhsa_system_sgpr_workgroup_info 0
		.amdhsa_system_vgpr_workitem_id 0
		.amdhsa_next_free_vgpr 492
		.amdhsa_next_free_sgpr 96
		.amdhsa_accum_offset 236
		.amdhsa_reserve_vcc 1
		.amdhsa_float_round_mode_32 0
		.amdhsa_float_round_mode_16_64 0
		.amdhsa_float_denorm_mode_32 3
		.amdhsa_float_denorm_mode_16_64 3
		.amdhsa_dx10_clamp 1
		.amdhsa_ieee_mode 1
		.amdhsa_fp16_overflow 0
		.amdhsa_tg_split 0
		.amdhsa_exception_fp_ieee_invalid_op 0
		.amdhsa_exception_fp_denorm_src 0
		.amdhsa_exception_fp_ieee_div_zero 0
		.amdhsa_exception_fp_ieee_overflow 0
		.amdhsa_exception_fp_ieee_underflow 0
		.amdhsa_exception_fp_ieee_inexact 0
		.amdhsa_exception_int_div_zero 0
	.end_amdhsa_kernel

amdhsa.kernels:
  - .agpr_count:     0
    .args:
      - .actual_access:  read_only
        .address_space:  global
        .offset:         0
        .size:           8
        .value_kind:     global_buffer
      - .address_space:  global
        .offset:         8
        .size:           8
        .value_kind:     global_buffer
      - .actual_access:  read_only
        .address_space:  global
        .offset:         16
        .size:           8
        .value_kind:     global_buffer
      - .actual_access:  read_only
        .address_space:  global
        .offset:         24
        .size:           8
        .value_kind:     global_buffer
      - .actual_access:  read_only
        .address_space:  global
        .offset:         32
        .size:           8
        .value_kind:     global_buffer
      - .actual_access:  read_only
        .address_space:  global
        .offset:         40
        .size:           8
        .value_kind:     global_buffer
      - .actual_access:  read_only
        .address_space:  global
        .offset:         48
        .size:           8
        .value_kind:     global_buffer
      - .actual_access:  read_only
        .address_space:  global
        .offset:         56
        .size:           8
        .value_kind:     global_buffer
      - .actual_access:  write_only
        .address_space:  global
        .offset:         64
        .size:           8
        .value_kind:     global_buffer
      - .actual_access:  write_only
        .address_space:  global
        .offset:         72
        .size:           8
        .value_kind:     global_buffer
      - .actual_access:  write_only
        .address_space:  global
        .offset:         80
        .size:           8
        .value_kind:     global_buffer
      - .actual_access:  write_only
        .address_space:  global
        .offset:         88
        .size:           8
        .value_kind:     global_buffer
      - .actual_access:  read_only
        .address_space:  global
        .offset:         96
        .size:           8
        .value_kind:     global_buffer
      - .actual_access:  write_only
        .address_space:  global
        .offset:         104
        .size:           8
        .value_kind:     global_buffer
      - .actual_access:  read_only
        .address_space:  global
        .offset:         112
        .size:           8
        .value_kind:     global_buffer
      - .actual_access:  write_only
        .address_space:  global
        .offset:         120
        .size:           8
        .value_kind:     global_buffer
      - .actual_access:  write_only
        .address_space:  global
        .offset:         128
        .size:           8
        .value_kind:     global_buffer
      - .actual_access:  write_only
        .address_space:  global
        .offset:         136
        .size:           8
        .value_kind:     global_buffer
      - .actual_access:  write_only
        .address_space:  global
        .offset:         144
        .size:           8
        .value_kind:     global_buffer
    .group_segment_fixed_size: 4096
    .kernarg_segment_align: 8
    .kernarg_segment_size: 152
    .language:       OpenCL C
    .language_version:
      - 2
      - 0
    .max_flat_workgroup_size: 512
    .name:           _Z7k_frontPKfPmS0_S0_S0_S0_S0_S0_PDF16_S2_PfS3_S0_S2_S0_S2_S3_S3_S3_
    .private_segment_fixed_size: 0
    .sgpr_count:     88
    .sgpr_spill_count: 0
    .symbol:         _Z7k_frontPKfPmS0_S0_S0_S0_S0_S0_PDF16_S2_PfS3_S0_S2_S0_S2_S3_S3_S3_.kd
    .uniform_work_group_size: 1
    .uses_dynamic_stack: false
    .vgpr_count:     68
    .vgpr_spill_count: 0
    .wavefront_size: 64
  - .agpr_count:     256
    .args:
      - .actual_access:  read_only
        .address_space:  global
        .offset:         0
        .size:           8
        .value_kind:     global_buffer
      - .actual_access:  read_only
        .address_space:  global
        .offset:         8
        .size:           8
        .value_kind:     global_buffer
      - .actual_access:  read_only
        .address_space:  global
        .offset:         16
        .size:           8
        .value_kind:     global_buffer
      - .actual_access:  read_only
        .address_space:  global
        .offset:         24
        .size:           8
        .value_kind:     global_buffer
      - .actual_access:  read_only
        .address_space:  global
        .offset:         32
        .size:           8
        .value_kind:     global_buffer
      - .address_space:  global
        .offset:         40
        .size:           8
        .value_kind:     global_buffer
      - .actual_access:  write_only
        .address_space:  global
        .offset:         48
        .size:           8
        .value_kind:     global_buffer
      - .actual_access:  write_only
        .address_space:  global
        .offset:         56
        .size:           8
        .value_kind:     global_buffer
    .group_segment_fixed_size: 114688
    .kernarg_segment_align: 8
    .kernarg_segment_size: 64
    .language:       OpenCL C
    .language_version:
      - 2
      - 0
    .max_flat_workgroup_size: 256
    .name:           _Z6k_mainPKDF16_PKfS2_S2_PKmPjPfS6_
    .private_segment_fixed_size: 0
    .sgpr_count:     99
    .sgpr_spill_count: 0
    .symbol:         _Z6k_mainPKDF16_PKfS2_S2_PKmPjPfS6_.kd
    .uniform_work_group_size: 1
    .uses_dynamic_stack: false
    .vgpr_count:     492
    .vgpr_spill_count: 0
    .wavefront_size: 64
  - .agpr_count:     0
    .args:
      - .actual_access:  read_only
        .address_space:  global
        .offset:         0
        .size:           8
        .value_kind:     global_buffer
      - .actual_access:  read_only
        .address_space:  global
        .offset:         8
        .size:           8
        .value_kind:     global_buffer
      - .actual_access:  read_only
        .address_space:  global
        .offset:         16
        .size:           8
        .value_kind:     global_buffer
      - .actual_access:  read_only
        .address_space:  global
        .offset:         24
        .size:           8
        .value_kind:     global_buffer
      - .actual_access:  read_only
        .address_space:  global
        .offset:         32
        .size:           8
        .value_kind:     global_buffer
      - .actual_access:  read_only
        .address_space:  global
        .offset:         40
        .size:           8
        .value_kind:     global_buffer
      - .actual_access:  read_only
        .address_space:  global
        .offset:         48
        .size:           8
        .value_kind:     global_buffer
      - .actual_access:  read_only
        .address_space:  global
        .offset:         56
        .size:           8
        .value_kind:     global_buffer
      - .actual_access:  read_only
        .address_space:  global
        .offset:         64
        .size:           8
        .value_kind:     global_buffer
      - .actual_access:  write_only
        .address_space:  global
        .offset:         72
        .size:           8
        .value_kind:     global_buffer
      - .actual_access:  write_only
        .address_space:  global
        .offset:         80
        .size:           8
        .value_kind:     global_buffer
    .group_segment_fixed_size: 101632
    .kernarg_segment_align: 8
    .kernarg_segment_size: 88
    .language:       OpenCL C
    .language_version:
      - 2
      - 0
    .max_flat_workgroup_size: 256
    .name:           _Z7k_graphPKfS0_S0_S0_S0_S0_S0_S0_S0_PfS1_
    .private_segment_fixed_size: 0
    .sgpr_count:     25
    .sgpr_spill_count: 0
    .symbol:         _Z7k_graphPKfS0_S0_S0_S0_S0_S0_S0_S0_PfS1_.kd
    .uniform_work_group_size: 1
    .uses_dynamic_stack: false
    .vgpr_count:     118
    .vgpr_spill_count: 0
    .wavefront_size: 64
  - .agpr_count:     0
    .args:
      - .actual_access:  read_only
        .address_space:  global
        .offset:         0
        .size:           8
        .value_kind:     global_buffer
      - .actual_access:  read_only
        .address_space:  global
        .offset:         8
        .size:           8
        .value_kind:     global_buffer
      - .actual_access:  read_only
        .address_space:  global
        .offset:         16
        .size:           8
        .value_kind:     global_buffer
      - .actual_access:  read_only
        .address_space:  global
        .offset:         24
        .size:           8
        .value_kind:     global_buffer
      - .actual_access:  read_only
        .address_space:  global
        .offset:         32
        .size:           8
        .value_kind:     global_buffer
      - .actual_access:  read_only
        .address_space:  global
        .offset:         40
        .size:           8
        .value_kind:     global_buffer
      - .actual_access:  read_only
        .address_space:  global
        .offset:         48
        .size:           8
        .value_kind:     global_buffer
      - .address_space:  global
        .offset:         56
        .size:           8
        .value_kind:     global_buffer
      - .actual_access:  read_only
        .address_space:  global
        .offset:         64
        .size:           8
        .value_kind:     global_buffer
      - .actual_access:  read_only
        .address_space:  global
        .offset:         72
        .size:           8
        .value_kind:     global_buffer
      - .actual_access:  read_only
        .address_space:  global
        .offset:         80
        .size:           8
        .value_kind:     global_buffer
      - .address_space:  global
        .offset:         88
        .size:           8
        .value_kind:     global_buffer
      - .actual_access:  write_only
        .address_space:  global
        .offset:         96
        .size:           8
        .value_kind:     global_buffer
      - .actual_access:  write_only
        .address_space:  global
        .offset:         104
        .size:           8
        .value_kind:     global_buffer
      - .actual_access:  write_only
        .address_space:  global
        .offset:         112
        .size:           8
        .value_kind:     global_buffer
      - .actual_access:  read_only
        .address_space:  global
        .offset:         120
        .size:           8
        .value_kind:     global_buffer
      - .actual_access:  read_only
        .address_space:  global
        .offset:         128
        .size:           8
        .value_kind:     global_buffer
      - .actual_access:  read_only
        .address_space:  global
        .offset:         136
        .size:           8
        .value_kind:     global_buffer
      - .actual_access:  read_only
        .address_space:  global
        .offset:         144
        .size:           8
        .value_kind:     global_buffer
      - .actual_access:  read_only
        .address_space:  global
        .offset:         152
        .size:           8
        .value_kind:     global_buffer
      - .actual_access:  read_only
        .address_space:  global
        .offset:         160
        .size:           8
        .value_kind:     global_buffer
      - .actual_access:  read_only
        .address_space:  global
        .offset:         168
        .size:           8
        .value_kind:     global_buffer
    .group_segment_fixed_size: 53792
    .kernarg_segment_align: 8
    .kernarg_segment_size: 176
    .language:       OpenCL C
    .language_version:
      - 2
      - 0
    .max_flat_workgroup_size: 512
    .name:           _Z9k_redprepILi1EEvPKfPKjS1_S1_S1_S1_S1_PfPKDv8_DF16_S7_S1_PDF16_S4_S4_S4_PKiS7_S1_S1_S1_S4_S4_
    .private_segment_fixed_size: 0
    .sgpr_count:     106
    .sgpr_spill_count: 4
    .symbol:         _Z9k_redprepILi1EEvPKfPKjS1_S1_S1_S1_S1_PfPKDv8_DF16_S7_S1_PDF16_S4_S4_S4_PKiS7_S1_S1_S1_S4_S4_.kd
    .uniform_work_group_size: 1
    .uses_dynamic_stack: false
    .vgpr_count:     103
    .vgpr_spill_count: 0
    .wavefront_size: 64
  - .agpr_count:     0
    .args:
      - .actual_access:  read_only
        .address_space:  global
        .offset:         0
        .size:           8
        .value_kind:     global_buffer
      - .actual_access:  read_only
        .address_space:  global
        .offset:         8
        .size:           8
        .value_kind:     global_buffer
      - .actual_access:  read_only
        .address_space:  global
        .offset:         16
        .size:           8
        .value_kind:     global_buffer
      - .actual_access:  read_only
        .address_space:  global
        .offset:         24
        .size:           8
        .value_kind:     global_buffer
      - .actual_access:  read_only
        .address_space:  global
        .offset:         32
        .size:           8
        .value_kind:     global_buffer
      - .actual_access:  read_only
        .address_space:  global
        .offset:         40
        .size:           8
        .value_kind:     global_buffer
      - .actual_access:  read_only
        .address_space:  global
        .offset:         48
        .size:           8
        .value_kind:     global_buffer
      - .address_space:  global
        .offset:         56
        .size:           8
        .value_kind:     global_buffer
      - .actual_access:  read_only
        .address_space:  global
        .offset:         64
        .size:           8
        .value_kind:     global_buffer
      - .actual_access:  read_only
        .address_space:  global
        .offset:         72
        .size:           8
        .value_kind:     global_buffer
      - .actual_access:  read_only
        .address_space:  global
        .offset:         80
        .size:           8
        .value_kind:     global_buffer
      - .actual_access:  read_only
        .address_space:  global
        .offset:         88
        .size:           8
        .value_kind:     global_buffer
      - .actual_access:  read_only
        .address_space:  global
        .offset:         96
        .size:           8
        .value_kind:     global_buffer
      - .actual_access:  read_only
        .address_space:  global
        .offset:         104
        .size:           8
        .value_kind:     global_buffer
      - .actual_access:  read_only
        .address_space:  global
        .offset:         112
        .size:           8
        .value_kind:     global_buffer
      - .actual_access:  read_only
        .address_space:  global
        .offset:         120
        .size:           8
        .value_kind:     global_buffer
      - .actual_access:  read_only
        .address_space:  global
        .offset:         128
        .size:           8
        .value_kind:     global_buffer
      - .actual_access:  read_only
        .address_space:  global
        .offset:         136
        .size:           8
        .value_kind:     global_buffer
      - .actual_access:  read_only
        .address_space:  global
        .offset:         144
        .size:           8
        .value_kind:     global_buffer
      - .actual_access:  read_only
        .address_space:  global
        .offset:         152
        .size:           8
        .value_kind:     global_buffer
      - .actual_access:  write_only
        .address_space:  global
        .offset:         160
        .size:           8
        .value_kind:     global_buffer
      - .address_space:  global
        .offset:         168
        .size:           8
        .value_kind:     global_buffer
    .group_segment_fixed_size: 66688
    .kernarg_segment_align: 8
    .kernarg_segment_size: 176
    .language:       OpenCL C
    .language_version:
      - 2
      - 0
    .max_flat_workgroup_size: 512
    .name:           _Z9k_redprepILi2EEvPKfPKjS1_S1_S1_S1_S1_PfPKDv8_DF16_S7_S1_PDF16_S4_S4_S4_PKiS7_S1_S1_S1_S4_S4_
    .private_segment_fixed_size: 0
    .sgpr_count:     102
    .sgpr_spill_count: 0
    .symbol:         _Z9k_redprepILi2EEvPKfPKjS1_S1_S1_S1_S1_PfPKDv8_DF16_S7_S1_PDF16_S4_S4_S4_PKiS7_S1_S1_S1_S4_S4_.kd
    .uniform_work_group_size: 1
    .uses_dynamic_stack: false
    .vgpr_count:     106
    .vgpr_spill_count: 0
    .wavefront_size: 64
